# speedup vs baseline: 1.0110x; 1.0039x over previous
.LBB1_3:
	s_waitcnt lgkmcnt(0)
	v_mfma_f32_32x32x16_f16 a[0:15], v[18:21], v[74:77], a[0:15]
	s_add_i32 s31, s30, 1
	s_cmp_lg_u32 s30, 2
	s_cselect_b32 s91, s31, 0
	s_mul_i32 s30, s30, 0x9000
	s_mul_i32 s92, s91, 0x9000
	s_add_i32 s96, s92, 0x9000
	s_cmp_lg_u32 s91, 2
	s_cselect_b32 s96, s96, 0
	s_add_i32 s96, s96, s93
	s_mov_b32 m0, s96
	v_add_u32_e32 v147, s30, v208
	global_load_lds_dwordx4 v164, s[94:95]
	s_add_u32 m0, s96, 0x1000
	v_add_u32_e32 v2, s30, v209
	global_load_lds_dwordx4 v165, s[94:95]
	s_add_u32 m0, s96, 0x2000
	v_add_u32_e32 v3, s30, v210
	global_load_lds_dwordx4 v166, s[94:95]
	s_add_u32 m0, s96, 0x3000
	v_add_u32_e32 v146, s92, v141
	global_load_lds_dwordx4 v167, s[94:95]
	s_add_u32 s30, s35, s20
	s_addc_u32 s31, s84, s21
	s_add_u32 m0, s96, 0x4000
	s_load_dwordx16 s[68:83], s[30:31], 0x80
	global_load_lds_dwordx4 v168, s[94:95]
	s_add_u32 m0, s96, 0x5000
	s_load_dwordx16 s[52:67], s[30:31], 0x8080
	global_load_lds_dwordx4 v169, s[94:95]
	s_add_u32 m0, s96, 0x6000
	ds_read_b128 v[90:93], v145
	global_load_lds_dwordx4 v170, s[94:95]
	s_add_u32 m0, s96, 0x7000
	ds_read_b128 v[82:85], v145 offset:2048
	global_load_lds_dwordx4 v171, s[94:95]
	v_mfma_f32_32x32x16_f16 a[240:255], v[38:41], v[74:77], a[240:255]
	ds_read_b128 v[50:53], v147
	v_pk_mul_f16 v148, v46, v136
	v_pk_mul_f16 v149, v42, v137
	v_pk_mul_f16 v150, v47, v136
	v_pk_mul_f16 v151, v43, v137
	v_mfma_f32_32x32x16_f16 a[16:31], v[18:21], v[126:129], a[16:31]
	ds_read_b128 v[54:57], v147 offset:4096
	v_pk_mul_f16 v152, v48, v136
	v_pk_mul_f16 v153, v44, v137
	v_pk_mul_f16 v154, v49, v136
	v_pk_mul_f16 v155, v45, v137
	v_mfma_f32_32x32x16_f16 a[224:239], v[38:41], v[126:129], a[224:239]
	ds_read_b128 v[58:61], v147 offset:8192
	v_pk_mul_f16 v156, v46, v140
	v_pk_mul_f16 v157, v42, v139
	v_pk_mul_f16 v158, v47, v140
	v_pk_mul_f16 v159, v43, v139
	v_mfma_f32_32x32x16_f16 a[32:47], v[18:21], v[122:125], a[32:47]
	ds_read_b128 v[62:65], v147 offset:12288
	v_pk_mul_f16 v160, v48, v140
	v_pk_mul_f16 v161, v44, v139
	v_pk_mul_f16 v162, v49, v140
	v_pk_mul_f16 v163, v45, v139
	v_mfma_f32_32x32x16_f16 a[208:223], v[38:41], v[122:125], a[208:223]
	ds_read_b128 v[66:69], v147 offset:16384
	v_pk_max_f16 v148, v148, v149
	v_pk_max_f16 v150, v150, v151
	v_pk_max_f16 v152, v152, v153
	v_pk_max_f16 v154, v154, v155
	v_mfma_f32_32x32x16_f16 a[48:63], v[18:21], v[118:121], a[48:63]
	ds_read_b128 v[70:73], v147 offset:20480
	v_pk_max_f16 v156, v156, v157
	v_pk_max_f16 v158, v158, v159
	v_pk_max_f16 v160, v160, v161
	v_pk_max_f16 v162, v162, v163
	v_mfma_f32_32x32x16_f16 a[192:207], v[38:41], v[118:121], a[192:207]
	ds_read_b128 v[78:81], v147 offset:24576
	v_cndmask_b32_e64 v114, v1, v148, s[36:37]
	s_mov_b64 vcc, s[38:39]
	v_cndmask_b32_sdwa v114, v1, v148, vcc dst_sel:WORD_1 dst_unused:UNUSED_PRESERVE src0_sel:WORD_1 src1_sel:WORD_1
	v_cndmask_b32_e64 v115, v1, v150, s[40:41]
	s_mov_b64 vcc, s[42:43]
	v_cndmask_b32_sdwa v115, v1, v150, vcc dst_sel:WORD_1 dst_unused:UNUSED_PRESERVE src0_sel:WORD_1 src1_sel:WORD_1
	v_mfma_f32_32x32x16_f16 a[64:79], v[18:21], v[106:109], a[64:79]
	ds_read_b128 v[102:105], v147 offset:28672
	v_cndmask_b32_e64 v116, v1, v152, s[44:45]
	s_mov_b64 vcc, s[46:47]
	v_cndmask_b32_sdwa v116, v1, v152, vcc dst_sel:WORD_1 dst_unused:UNUSED_PRESERVE src0_sel:WORD_1 src1_sel:WORD_1
	v_cndmask_b32_e64 v117, v1, v154, s[48:49]
	s_mov_b64 vcc, s[50:51]
	v_cndmask_b32_sdwa v117, v1, v154, vcc dst_sel:WORD_1 dst_unused:UNUSED_PRESERVE src0_sel:WORD_1 src1_sel:WORD_1
	v_mfma_f32_32x32x16_f16 a[176:191], v[38:41], v[106:109], a[176:191]
	v_cndmask_b32_e64 v110, v138, v156, s[4:5]
	s_mov_b64 vcc, s[6:7]
	v_cndmask_b32_sdwa v110, v138, v156, vcc dst_sel:WORD_1 dst_unused:UNUSED_PRESERVE src0_sel:WORD_1 src1_sel:WORD_1
	v_cndmask_b32_e64 v111, v138, v158, s[8:9]
	s_mov_b64 vcc, s[10:11]
	v_cndmask_b32_sdwa v111, v138, v158, vcc dst_sel:WORD_1 dst_unused:UNUSED_PRESERVE src0_sel:WORD_1 src1_sel:WORD_1
	v_mfma_f32_32x32x16_f16 a[112:127], v[18:21], v[98:101], a[112:127]
	v_cndmask_b32_e64 v112, v138, v160, s[12:13]
	s_mov_b64 vcc, s[14:15]
	v_cndmask_b32_sdwa v112, v138, v160, vcc dst_sel:WORD_1 dst_unused:UNUSED_PRESERVE src0_sel:WORD_1 src1_sel:WORD_1
	v_cndmask_b32_e64 v113, v138, v162, s[16:17]
	s_mov_b64 vcc, s[18:19]
	v_cndmask_b32_sdwa v113, v138, v162, vcc dst_sel:WORD_1 dst_unused:UNUSED_PRESERVE src0_sel:WORD_1 src1_sel:WORD_1
	v_mfma_f32_32x32x16_f16 a[160:175], v[38:41], v[98:101], a[160:175]
	v_pk_add_f16 v148, v115, v114
	v_pk_add_f16 v149, v116, v117
	v_mfma_f32_32x32x16_f16 a[128:143], v[18:21], v[94:97], a[128:143]
	v_pk_add_f16 v150, v111, v110
	v_pk_add_f16 v151, v112, v113
	v_mfma_f32_32x32x16_f16 a[144:159], v[38:41], v[94:97], a[144:159]
	v_pk_add_f16 v148, v148, v149
	v_pk_add_f16 v150, v150, v151
	v_mfma_f32_32x32x16_f16 a[80:95], v[18:21], v[86:89], a[80:95]
	v_fma_mix_f32 v134, v148, 1.0, v134 op_sel_hi:[1,0,0]
	v_fma_mix_f32 v135, v150, 1.0, v135 op_sel_hi:[1,0,0]
	v_mfma_f32_32x32x16_f16 a[96:111], v[38:41], v[86:89], a[96:111]
	v_fma_mix_f32 v134, v148, 1.0, v134 op_sel:[1,0,0] op_sel_hi:[1,0,0]
	v_fma_mix_f32 v135, v150, 1.0, v135 op_sel:[1,0,0] op_sel_hi:[1,0,0]
	s_waitcnt lgkmcnt(0)
	v_mfma_f32_32x32x16_f16 a[0:15], v[114:117], v[50:53], a[0:15]
	s_load_dwordx16 s[36:51], s[30:31], 0xc0
	s_load_dwordx16 s[4:19], s[30:31], 0x80c0
	ds_read_b128 v[46:49], v145 offset:32
	ds_read_b128 v[42:45], v145 offset:2080
	v_mfma_f32_32x32x16_f16 a[240:255], v[110:113], v[50:53], a[240:255]
	ds_read_b128 v[74:77], v2
	v_pk_mul_f16 v148, v90, v136
	v_pk_mul_f16 v149, v82, v137
	v_pk_mul_f16 v150, v91, v136
	v_pk_mul_f16 v151, v83, v137
	v_mfma_f32_32x32x16_f16 a[16:31], v[114:117], v[54:57], a[16:31]
	ds_read_b128 v[126:129], v2 offset:4096
	v_pk_mul_f16 v152, v92, v136
	v_pk_mul_f16 v153, v84, v137
	v_pk_mul_f16 v154, v93, v136
	v_pk_mul_f16 v155, v85, v137
	v_mfma_f32_32x32x16_f16 a[224:239], v[110:113], v[54:57], a[224:239]
	ds_read_b128 v[122:125], v2 offset:8192
	v_pk_mul_f16 v156, v90, v140
	v_pk_mul_f16 v157, v82, v139
	v_pk_mul_f16 v158, v91, v140
	v_pk_mul_f16 v159, v83, v139
	v_mfma_f32_32x32x16_f16 a[32:47], v[114:117], v[58:61], a[32:47]
	ds_read_b128 v[118:121], v2 offset:12288
	v_pk_mul_f16 v160, v92, v140
	v_pk_mul_f16 v161, v84, v139
	v_pk_mul_f16 v162, v93, v140
	v_pk_mul_f16 v163, v85, v139
	v_mfma_f32_32x32x16_f16 a[208:223], v[110:113], v[58:61], a[208:223]
	ds_read_b128 v[106:109], v2 offset:16384
	v_pk_max_f16 v148, v148, v149
	v_pk_max_f16 v150, v150, v151
	v_pk_max_f16 v152, v152, v153
	v_pk_max_f16 v154, v154, v155
	v_mfma_f32_32x32x16_f16 a[48:63], v[114:117], v[62:65], a[48:63]
	ds_read_b128 v[98:101], v2 offset:20480
	v_pk_max_f16 v156, v156, v157
	v_pk_max_f16 v158, v158, v159
	v_pk_max_f16 v160, v160, v161
	v_pk_max_f16 v162, v162, v163
	v_mfma_f32_32x32x16_f16 a[192:207], v[110:113], v[62:65], a[192:207]
	ds_read_b128 v[94:97], v2 offset:24576
	v_cndmask_b32_e64 v18, v1, v148, s[68:69]
	s_mov_b64 vcc, s[70:71]
	v_cndmask_b32_sdwa v18, v1, v148, vcc dst_sel:WORD_1 dst_unused:UNUSED_PRESERVE src0_sel:WORD_1 src1_sel:WORD_1
	v_cndmask_b32_e64 v19, v1, v150, s[72:73]
	s_mov_b64 vcc, s[74:75]
	v_cndmask_b32_sdwa v19, v1, v150, vcc dst_sel:WORD_1 dst_unused:UNUSED_PRESERVE src0_sel:WORD_1 src1_sel:WORD_1
	v_mfma_f32_32x32x16_f16 a[64:79], v[114:117], v[66:69], a[64:79]
	ds_read_b128 v[86:89], v2 offset:28672
	v_cndmask_b32_e64 v20, v1, v152, s[76:77]
	s_mov_b64 vcc, s[78:79]
	v_cndmask_b32_sdwa v20, v1, v152, vcc dst_sel:WORD_1 dst_unused:UNUSED_PRESERVE src0_sel:WORD_1 src1_sel:WORD_1
	v_cndmask_b32_e64 v21, v1, v154, s[80:81]
	s_mov_b64 vcc, s[82:83]
	v_cndmask_b32_sdwa v21, v1, v154, vcc dst_sel:WORD_1 dst_unused:UNUSED_PRESERVE src0_sel:WORD_1 src1_sel:WORD_1
	v_mfma_f32_32x32x16_f16 a[176:191], v[110:113], v[66:69], a[176:191]
	v_cndmask_b32_e64 v38, v138, v156, s[52:53]
	s_mov_b64 vcc, s[54:55]
	v_cndmask_b32_sdwa v38, v138, v156, vcc dst_sel:WORD_1 dst_unused:UNUSED_PRESERVE src0_sel:WORD_1 src1_sel:WORD_1
	v_cndmask_b32_e64 v39, v138, v158, s[56:57]
	s_mov_b64 vcc, s[58:59]
	v_cndmask_b32_sdwa v39, v138, v158, vcc dst_sel:WORD_1 dst_unused:UNUSED_PRESERVE src0_sel:WORD_1 src1_sel:WORD_1
	v_mfma_f32_32x32x16_f16 a[112:127], v[114:117], v[70:73], a[112:127]
	v_cndmask_b32_e64 v40, v138, v160, s[60:61]
	s_mov_b64 vcc, s[62:63]
	v_cndmask_b32_sdwa v40, v138, v160, vcc dst_sel:WORD_1 dst_unused:UNUSED_PRESERVE src0_sel:WORD_1 src1_sel:WORD_1
	v_cndmask_b32_e64 v41, v138, v162, s[64:65]
	s_mov_b64 vcc, s[66:67]
	v_cndmask_b32_sdwa v41, v138, v162, vcc dst_sel:WORD_1 dst_unused:UNUSED_PRESERVE src0_sel:WORD_1 src1_sel:WORD_1
	v_mfma_f32_32x32x16_f16 a[160:175], v[110:113], v[70:73], a[160:175]
	v_pk_add_f16 v148, v19, v18
	v_pk_add_f16 v149, v20, v21
	v_mfma_f32_32x32x16_f16 a[128:143], v[114:117], v[78:81], a[128:143]
	v_pk_add_f16 v150, v39, v38
	v_pk_add_f16 v151, v40, v41
	v_mfma_f32_32x32x16_f16 a[144:159], v[110:113], v[78:81], a[144:159]
	v_pk_add_f16 v148, v148, v149
	v_pk_add_f16 v150, v150, v151
	v_mfma_f32_32x32x16_f16 a[80:95], v[114:117], v[102:105], a[80:95]
	v_fma_mix_f32 v134, v148, 1.0, v134 op_sel_hi:[1,0,0]
	v_fma_mix_f32 v135, v150, 1.0, v135 op_sel_hi:[1,0,0]
	v_mfma_f32_32x32x16_f16 a[96:111], v[110:113], v[102:105], a[96:111]
	v_fma_mix_f32 v134, v148, 1.0, v134 op_sel:[1,0,0] op_sel_hi:[1,0,0]
	v_fma_mix_f32 v135, v150, 1.0, v135 op_sel:[1,0,0] op_sel_hi:[1,0,0]
	s_waitcnt lgkmcnt(0)
	v_mfma_f32_32x32x16_f16 a[0:15], v[18:21], v[74:77], a[0:15]
	s_load_dwordx16 s[68:83], s[30:31], 0x100
	s_load_dwordx16 s[52:67], s[30:31], 0x8100
	ds_read_b128 v[90:93], v145 offset:64
	ds_read_b128 v[82:85], v145 offset:2112
	v_mfma_f32_32x32x16_f16 a[240:255], v[38:41], v[74:77], a[240:255]
	ds_read_b128 v[50:53], v3
	v_pk_mul_f16 v148, v46, v136
	v_pk_mul_f16 v149, v42, v137
	v_pk_mul_f16 v150, v47, v136
	v_pk_mul_f16 v151, v43, v137
	v_mfma_f32_32x32x16_f16 a[16:31], v[18:21], v[126:129], a[16:31]
	ds_read_b128 v[54:57], v3 offset:4096
	v_pk_mul_f16 v152, v48, v136
	v_pk_mul_f16 v153, v44, v137
	v_pk_mul_f16 v154, v49, v136
	v_pk_mul_f16 v155, v45, v137
	v_mfma_f32_32x32x16_f16 a[224:239], v[38:41], v[126:129], a[224:239]
	ds_read_b128 v[58:61], v3 offset:8192
	v_pk_mul_f16 v156, v46, v140
	v_pk_mul_f16 v157, v42, v139
	v_pk_mul_f16 v158, v47, v140
	v_pk_mul_f16 v159, v43, v139
	v_mfma_f32_32x32x16_f16 a[32:47], v[18:21], v[122:125], a[32:47]
	ds_read_b128 v[62:65], v3 offset:12288
	v_pk_mul_f16 v160, v48, v140
	v_pk_mul_f16 v161, v44, v139
	v_pk_mul_f16 v162, v49, v140
	v_pk_mul_f16 v163, v45, v139
	v_mfma_f32_32x32x16_f16 a[208:223], v[38:41], v[122:125], a[208:223]
	ds_read_b128 v[66:69], v3 offset:16384
	v_pk_max_f16 v148, v148, v149
	v_pk_max_f16 v150, v150, v151
	v_pk_max_f16 v152, v152, v153
	v_pk_max_f16 v154, v154, v155
	v_mfma_f32_32x32x16_f16 a[48:63], v[18:21], v[118:121], a[48:63]
	ds_read_b128 v[70:73], v3 offset:20480
	v_pk_max_f16 v156, v156, v157
	v_pk_max_f16 v158, v158, v159
	v_pk_max_f16 v160, v160, v161
	v_pk_max_f16 v162, v162, v163
	v_mfma_f32_32x32x16_f16 a[192:207], v[38:41], v[118:121], a[192:207]
	ds_read_b128 v[78:81], v3 offset:24576
	v_cndmask_b32_e64 v114, v1, v148, s[36:37]
	s_mov_b64 vcc, s[38:39]
	v_cndmask_b32_sdwa v114, v1, v148, vcc dst_sel:WORD_1 dst_unused:UNUSED_PRESERVE src0_sel:WORD_1 src1_sel:WORD_1
	v_cndmask_b32_e64 v115, v1, v150, s[40:41]
	s_mov_b64 vcc, s[42:43]
	v_cndmask_b32_sdwa v115, v1, v150, vcc dst_sel:WORD_1 dst_unused:UNUSED_PRESERVE src0_sel:WORD_1 src1_sel:WORD_1
	v_mfma_f32_32x32x16_f16 a[64:79], v[18:21], v[106:109], a[64:79]
	ds_read_b128 v[102:105], v3 offset:28672
	v_cndmask_b32_e64 v116, v1, v152, s[44:45]
	s_mov_b64 vcc, s[46:47]
	v_cndmask_b32_sdwa v116, v1, v152, vcc dst_sel:WORD_1 dst_unused:UNUSED_PRESERVE src0_sel:WORD_1 src1_sel:WORD_1
	v_cndmask_b32_e64 v117, v1, v154, s[48:49]
	s_mov_b64 vcc, s[50:51]
	v_cndmask_b32_sdwa v117, v1, v154, vcc dst_sel:WORD_1 dst_unused:UNUSED_PRESERVE src0_sel:WORD_1 src1_sel:WORD_1
	v_mfma_f32_32x32x16_f16 a[176:191], v[38:41], v[106:109], a[176:191]
	v_cndmask_b32_e64 v110, v138, v156, s[4:5]
	s_mov_b64 vcc, s[6:7]
	v_cndmask_b32_sdwa v110, v138, v156, vcc dst_sel:WORD_1 dst_unused:UNUSED_PRESERVE src0_sel:WORD_1 src1_sel:WORD_1
	v_cndmask_b32_e64 v111, v138, v158, s[8:9]
	s_mov_b64 vcc, s[10:11]
	v_cndmask_b32_sdwa v111, v138, v158, vcc dst_sel:WORD_1 dst_unused:UNUSED_PRESERVE src0_sel:WORD_1 src1_sel:WORD_1
	v_mfma_f32_32x32x16_f16 a[112:127], v[18:21], v[98:101], a[112:127]
	v_cndmask_b32_e64 v112, v138, v160, s[12:13]
	s_mov_b64 vcc, s[14:15]
	v_cndmask_b32_sdwa v112, v138, v160, vcc dst_sel:WORD_1 dst_unused:UNUSED_PRESERVE src0_sel:WORD_1 src1_sel:WORD_1
	v_cndmask_b32_e64 v113, v138, v162, s[16:17]
	s_mov_b64 vcc, s[18:19]
	v_cndmask_b32_sdwa v113, v138, v162, vcc dst_sel:WORD_1 dst_unused:UNUSED_PRESERVE src0_sel:WORD_1 src1_sel:WORD_1
	v_mfma_f32_32x32x16_f16 a[160:175], v[38:41], v[98:101], a[160:175]
	v_pk_add_f16 v148, v115, v114
	v_pk_add_f16 v149, v116, v117
	v_mfma_f32_32x32x16_f16 a[128:143], v[18:21], v[94:97], a[128:143]
	v_pk_add_f16 v150, v111, v110
	v_pk_add_f16 v151, v112, v113
	v_mfma_f32_32x32x16_f16 a[144:159], v[38:41], v[94:97], a[144:159]
	v_pk_add_f16 v148, v148, v149
	v_pk_add_f16 v150, v150, v151
	v_mfma_f32_32x32x16_f16 a[80:95], v[18:21], v[86:89], a[80:95]
	v_fma_mix_f32 v134, v148, 1.0, v134 op_sel_hi:[1,0,0]
	v_fma_mix_f32 v135, v150, 1.0, v135 op_sel_hi:[1,0,0]
	v_mfma_f32_32x32x16_f16 a[96:111], v[38:41], v[86:89], a[96:111]
	v_fma_mix_f32 v134, v148, 1.0, v134 op_sel:[1,0,0] op_sel_hi:[1,0,0]
	v_fma_mix_f32 v135, v150, 1.0, v135 op_sel:[1,0,0] op_sel_hi:[1,0,0]
	s_waitcnt lgkmcnt(0)
	v_mfma_f32_32x32x16_f16 a[0:15], v[114:117], v[50:53], a[0:15]
	s_load_dwordx16 s[36:51], s[30:31], 0x140
	s_load_dwordx16 s[4:19], s[30:31], 0x8140
	ds_read_b128 v[46:49], v145 offset:96
	ds_read_b128 v[42:45], v145 offset:2144
	v_mfma_f32_32x32x16_f16 a[240:255], v[110:113], v[50:53], a[240:255]
	ds_read_b128 v[74:77], v146
	v_pk_mul_f16 v148, v90, v136
	v_pk_mul_f16 v149, v82, v137
	v_pk_mul_f16 v150, v91, v136
	v_pk_mul_f16 v151, v83, v137
	v_mfma_f32_32x32x16_f16 a[16:31], v[114:117], v[54:57], a[16:31]
	ds_read_b128 v[126:129], v146 offset:4096
	v_pk_mul_f16 v152, v92, v136
	v_pk_mul_f16 v153, v84, v137
	v_pk_mul_f16 v154, v93, v136
	v_pk_mul_f16 v155, v85, v137
	v_mfma_f32_32x32x16_f16 a[224:239], v[110:113], v[54:57], a[224:239]
	ds_read_b128 v[122:125], v146 offset:8192
	v_pk_mul_f16 v156, v90, v140
	v_pk_mul_f16 v157, v82, v139
	v_pk_mul_f16 v158, v91, v140
	v_pk_mul_f16 v159, v83, v139
	v_mfma_f32_32x32x16_f16 a[32:47], v[114:117], v[58:61], a[32:47]
	ds_read_b128 v[118:121], v146 offset:12288
	v_pk_mul_f16 v160, v92, v140
	v_pk_mul_f16 v161, v84, v139
	v_pk_mul_f16 v162, v93, v140
	v_pk_mul_f16 v163, v85, v139
	v_mfma_f32_32x32x16_f16 a[208:223], v[110:113], v[58:61], a[208:223]
	ds_read_b128 v[106:109], v146 offset:16384
	v_pk_max_f16 v148, v148, v149
	v_pk_max_f16 v150, v150, v151
	v_pk_max_f16 v152, v152, v153
	v_pk_max_f16 v154, v154, v155
	v_mfma_f32_32x32x16_f16 a[48:63], v[114:117], v[62:65], a[48:63]
	ds_read_b128 v[98:101], v146 offset:20480
	v_pk_max_f16 v156, v156, v157
	v_pk_max_f16 v158, v158, v159
	v_pk_max_f16 v160, v160, v161
	v_pk_max_f16 v162, v162, v163
	v_mfma_f32_32x32x16_f16 a[192:207], v[110:113], v[62:65], a[192:207]
	ds_read_b128 v[94:97], v146 offset:24576
	v_cndmask_b32_e64 v18, v1, v148, s[68:69]
	s_mov_b64 vcc, s[70:71]
	v_cndmask_b32_sdwa v18, v1, v148, vcc dst_sel:WORD_1 dst_unused:UNUSED_PRESERVE src0_sel:WORD_1 src1_sel:WORD_1
	v_cndmask_b32_e64 v19, v1, v150, s[72:73]
	s_mov_b64 vcc, s[74:75]
	v_cndmask_b32_sdwa v19, v1, v150, vcc dst_sel:WORD_1 dst_unused:UNUSED_PRESERVE src0_sel:WORD_1 src1_sel:WORD_1
	v_mfma_f32_32x32x16_f16 a[64:79], v[114:117], v[66:69], a[64:79]
	ds_read_b128 v[86:89], v146 offset:28672
	v_cndmask_b32_e64 v20, v1, v152, s[76:77]
	s_mov_b64 vcc, s[78:79]
	v_cndmask_b32_sdwa v20, v1, v152, vcc dst_sel:WORD_1 dst_unused:UNUSED_PRESERVE src0_sel:WORD_1 src1_sel:WORD_1
	v_cndmask_b32_e64 v21, v1, v154, s[80:81]
	s_mov_b64 vcc, s[82:83]
	v_cndmask_b32_sdwa v21, v1, v154, vcc dst_sel:WORD_1 dst_unused:UNUSED_PRESERVE src0_sel:WORD_1 src1_sel:WORD_1
	v_mfma_f32_32x32x16_f16 a[176:191], v[110:113], v[66:69], a[176:191]
	v_cndmask_b32_e64 v38, v138, v156, s[52:53]
	s_mov_b64 vcc, s[54:55]
	v_cndmask_b32_sdwa v38, v138, v156, vcc dst_sel:WORD_1 dst_unused:UNUSED_PRESERVE src0_sel:WORD_1 src1_sel:WORD_1
	v_cndmask_b32_e64 v39, v138, v158, s[56:57]
	s_mov_b64 vcc, s[58:59]
	v_cndmask_b32_sdwa v39, v138, v158, vcc dst_sel:WORD_1 dst_unused:UNUSED_PRESERVE src0_sel:WORD_1 src1_sel:WORD_1
	v_mfma_f32_32x32x16_f16 a[112:127], v[114:117], v[70:73], a[112:127]
	v_cndmask_b32_e64 v40, v138, v160, s[60:61]
	s_mov_b64 vcc, s[62:63]
	v_cndmask_b32_sdwa v40, v138, v160, vcc dst_sel:WORD_1 dst_unused:UNUSED_PRESERVE src0_sel:WORD_1 src1_sel:WORD_1
	v_cndmask_b32_e64 v41, v138, v162, s[64:65]
	s_mov_b64 vcc, s[66:67]
	v_cndmask_b32_sdwa v41, v138, v162, vcc dst_sel:WORD_1 dst_unused:UNUSED_PRESERVE src0_sel:WORD_1 src1_sel:WORD_1
	v_mfma_f32_32x32x16_f16 a[160:175], v[110:113], v[70:73], a[160:175]
	v_pk_add_f16 v148, v19, v18
	v_pk_add_f16 v149, v20, v21
	v_mfma_f32_32x32x16_f16 a[128:143], v[114:117], v[78:81], a[128:143]
	v_pk_add_f16 v150, v39, v38
	v_pk_add_f16 v151, v40, v41
	v_mfma_f32_32x32x16_f16 a[144:159], v[110:113], v[78:81], a[144:159]
	v_pk_add_f16 v148, v148, v149
	v_pk_add_f16 v150, v150, v151
	v_mfma_f32_32x32x16_f16 a[80:95], v[114:117], v[102:105], a[80:95]
	v_fma_mix_f32 v134, v148, 1.0, v134 op_sel_hi:[1,0,0]
	v_fma_mix_f32 v135, v150, 1.0, v135 op_sel_hi:[1,0,0]
	v_mfma_f32_32x32x16_f16 a[96:111], v[110:113], v[102:105], a[96:111]
	v_fma_mix_f32 v134, v148, 1.0, v134 op_sel:[1,0,0] op_sel_hi:[1,0,0]
	v_fma_mix_f32 v135, v150, 1.0, v135 op_sel:[1,0,0] op_sel_hi:[1,0,0]
	s_add_i32 s92, s92, 0x9000
	s_cmp_lg_u32 s91, 2
	s_cselect_b32 s30, s92, 0
	s_add_u32 s20, s20, 0x100
	s_addc_u32 s21, s21, 0
	s_add_u32 s94, s94, 0x8000
	s_addc_u32 s95, s95, 0
	v_add_u32_e32 v145, 0x80, v145
	s_cmpk_eq_i32 s20, 0xf00
	s_mov_b32 s30, s91
	s_waitcnt vmcnt(0)
	s_waitcnt lgkmcnt(0)
	s_barrier
	s_cbranch_scc0 .LBB1_3
	s_waitcnt lgkmcnt(0)
	v_mfma_f32_32x32x16_f16 a[0:15], v[18:21], v[74:77], a[0:15]
	s_load_dwordx16 s[68:83], s[0:1], 0xf80
	s_load_dwordx16 s[52:67], s[0:1], 0x8f80
	ds_read_b128 v[90:93], v142 offset:1984
	ds_read_b128 v[82:85], v142 offset:4032
	v_mfma_f32_32x32x16_f16 a[240:255], v[38:41], v[74:77], a[240:255]
	ds_read_b128 v[50:53], v208
	v_pk_mul_f16 v148, v46, v136
	v_pk_mul_f16 v149, v42, v137
	v_pk_mul_f16 v150, v47, v136
	v_pk_mul_f16 v151, v43, v137
	v_mfma_f32_32x32x16_f16 a[16:31], v[18:21], v[126:129], a[16:31]
	ds_read_b128 v[54:57], v208 offset:4096
	v_pk_mul_f16 v152, v48, v136
	v_pk_mul_f16 v153, v44, v137
	v_pk_mul_f16 v154, v49, v136
	v_pk_mul_f16 v155, v45, v137
	v_mfma_f32_32x32x16_f16 a[224:239], v[38:41], v[126:129], a[224:239]
	ds_read_b128 v[58:61], v208 offset:8192
	v_pk_mul_f16 v156, v46, v140
	v_pk_mul_f16 v157, v42, v139
	v_pk_mul_f16 v158, v47, v140
	v_pk_mul_f16 v159, v43, v139
	v_mfma_f32_32x32x16_f16 a[32:47], v[18:21], v[122:125], a[32:47]
	ds_read_b128 v[62:65], v208 offset:12288
	v_pk_mul_f16 v160, v48, v140
	v_pk_mul_f16 v161, v44, v139
	v_pk_mul_f16 v162, v49, v140
	v_pk_mul_f16 v163, v45, v139
	v_mfma_f32_32x32x16_f16 a[208:223], v[38:41], v[122:125], a[208:223]
	ds_read_b128 v[66:69], v208 offset:16384
	v_pk_max_f16 v148, v148, v149
	v_pk_max_f16 v150, v150, v151
	v_pk_max_f16 v152, v152, v153
	v_pk_max_f16 v154, v154, v155
	v_mfma_f32_32x32x16_f16 a[48:63], v[18:21], v[118:121], a[48:63]
	ds_read_b128 v[70:73], v208 offset:20480
	v_pk_max_f16 v156, v156, v157
	v_pk_max_f16 v158, v158, v159
	v_pk_max_f16 v160, v160, v161
	v_pk_max_f16 v162, v162, v163
	v_mfma_f32_32x32x16_f16 a[192:207], v[38:41], v[118:121], a[192:207]
	ds_read_b128 v[78:81], v208 offset:24576
	v_cndmask_b32_e64 v114, v1, v148, s[36:37]
	s_mov_b64 vcc, s[38:39]
	v_cndmask_b32_sdwa v114, v1, v148, vcc dst_sel:WORD_1 dst_unused:UNUSED_PRESERVE src0_sel:WORD_1 src1_sel:WORD_1
	v_cndmask_b32_e64 v115, v1, v150, s[40:41]
	s_mov_b64 vcc, s[42:43]
	v_cndmask_b32_sdwa v115, v1, v150, vcc dst_sel:WORD_1 dst_unused:UNUSED_PRESERVE src0_sel:WORD_1 src1_sel:WORD_1
	v_mfma_f32_32x32x16_f16 a[64:79], v[18:21], v[106:109], a[64:79]
	ds_read_b128 v[102:105], v208 offset:28672
	v_cndmask_b32_e64 v116, v1, v152, s[44:45]
	s_mov_b64 vcc, s[46:47]
	v_cndmask_b32_sdwa v116, v1, v152, vcc dst_sel:WORD_1 dst_unused:UNUSED_PRESERVE src0_sel:WORD_1 src1_sel:WORD_1
	v_cndmask_b32_e64 v117, v1, v154, s[48:49]
	s_mov_b64 vcc, s[50:51]
	v_cndmask_b32_sdwa v117, v1, v154, vcc dst_sel:WORD_1 dst_unused:UNUSED_PRESERVE src0_sel:WORD_1 src1_sel:WORD_1
	v_mfma_f32_32x32x16_f16 a[176:191], v[38:41], v[106:109], a[176:191]
	v_cndmask_b32_e64 v110, v138, v156, s[4:5]
	s_mov_b64 vcc, s[6:7]
	v_cndmask_b32_sdwa v110, v138, v156, vcc dst_sel:WORD_1 dst_unused:UNUSED_PRESERVE src0_sel:WORD_1 src1_sel:WORD_1
	v_cndmask_b32_e64 v111, v138, v158, s[8:9]
	s_mov_b64 vcc, s[10:11]
	v_cndmask_b32_sdwa v111, v138, v158, vcc dst_sel:WORD_1 dst_unused:UNUSED_PRESERVE src0_sel:WORD_1 src1_sel:WORD_1
	v_mfma_f32_32x32x16_f16 a[112:127], v[18:21], v[98:101], a[112:127]
	v_cndmask_b32_e64 v112, v138, v160, s[12:13]
	s_mov_b64 vcc, s[14:15]
	v_cndmask_b32_sdwa v112, v138, v160, vcc dst_sel:WORD_1 dst_unused:UNUSED_PRESERVE src0_sel:WORD_1 src1_sel:WORD_1
	v_cndmask_b32_e64 v113, v138, v162, s[16:17]
	s_mov_b64 vcc, s[18:19]
	v_cndmask_b32_sdwa v113, v138, v162, vcc dst_sel:WORD_1 dst_unused:UNUSED_PRESERVE src0_sel:WORD_1 src1_sel:WORD_1
	v_mfma_f32_32x32x16_f16 a[160:175], v[38:41], v[98:101], a[160:175]
	v_pk_add_f16 v148, v115, v114
	v_pk_add_f16 v149, v116, v117
	v_mfma_f32_32x32x16_f16 a[128:143], v[18:21], v[94:97], a[128:143]
	v_pk_add_f16 v150, v111, v110
	v_pk_add_f16 v151, v112, v113
	v_mfma_f32_32x32x16_f16 a[144:159], v[38:41], v[94:97], a[144:159]
	v_pk_add_f16 v148, v148, v149
	v_pk_add_f16 v150, v150, v151
	v_mfma_f32_32x32x16_f16 a[80:95], v[18:21], v[86:89], a[80:95]
	v_fma_mix_f32 v134, v148, 1.0, v134 op_sel_hi:[1,0,0]
	v_fma_mix_f32 v135, v150, 1.0, v135 op_sel_hi:[1,0,0]
	v_mfma_f32_32x32x16_f16 a[96:111], v[38:41], v[86:89], a[96:111]
	v_fma_mix_f32 v134, v148, 1.0, v134 op_sel:[1,0,0] op_sel_hi:[1,0,0]
	v_fma_mix_f32 v135, v150, 1.0, v135 op_sel:[1,0,0] op_sel_hi:[1,0,0]
	s_waitcnt lgkmcnt(0)
	v_mfma_f32_32x32x16_f16 a[0:15], v[114:117], v[50:53], a[0:15]
	s_load_dwordx16 s[36:51], s[0:1], 0xfc0
	s_load_dwordx16 s[4:19], s[0:1], 0x8fc0
	ds_read_b128 v[46:49], v142 offset:2016
	ds_read_b128 v[42:45], v142 offset:4064
	v_mfma_f32_32x32x16_f16 a[240:255], v[110:113], v[50:53], a[240:255]
	ds_read_b128 v[74:77], v209
	v_pk_mul_f16 v148, v90, v136
	v_pk_mul_f16 v149, v82, v137
	v_pk_mul_f16 v150, v91, v136
	v_pk_mul_f16 v151, v83, v137
	v_mfma_f32_32x32x16_f16 a[16:31], v[114:117], v[54:57], a[16:31]
	ds_read_b128 v[126:129], v209 offset:4096
	v_pk_mul_f16 v152, v92, v136
	v_pk_mul_f16 v153, v84, v137
	v_pk_mul_f16 v154, v93, v136
	v_pk_mul_f16 v155, v85, v137
	v_mfma_f32_32x32x16_f16 a[224:239], v[110:113], v[54:57], a[224:239]
	ds_read_b128 v[122:125], v209 offset:8192
	v_pk_mul_f16 v156, v90, v140
	v_pk_mul_f16 v157, v82, v139
	v_pk_mul_f16 v158, v91, v140
	v_pk_mul_f16 v159, v83, v139
	v_mfma_f32_32x32x16_f16 a[32:47], v[114:117], v[58:61], a[32:47]
	ds_read_b128 v[118:121], v209 offset:12288
	v_pk_mul_f16 v160, v92, v140
	v_pk_mul_f16 v161, v84, v139
	v_pk_mul_f16 v162, v93, v140
	v_pk_mul_f16 v163, v85, v139
	v_mfma_f32_32x32x16_f16 a[208:223], v[110:113], v[58:61], a[208:223]
	ds_read_b128 v[106:109], v209 offset:16384
	v_pk_max_f16 v148, v148, v149
	v_pk_max_f16 v150, v150, v151
	v_pk_max_f16 v152, v152, v153
	v_pk_max_f16 v154, v154, v155
	v_mfma_f32_32x32x16_f16 a[48:63], v[114:117], v[62:65], a[48:63]
	ds_read_b128 v[98:101], v209 offset:20480
	v_pk_max_f16 v156, v156, v157
	v_pk_max_f16 v158, v158, v159
	v_pk_max_f16 v160, v160, v161
	v_pk_max_f16 v162, v162, v163
	v_mfma_f32_32x32x16_f16 a[192:207], v[110:113], v[62:65], a[192:207]
	ds_read_b128 v[94:97], v209 offset:24576
	v_cndmask_b32_e64 v18, v1, v148, s[68:69]
	s_mov_b64 vcc, s[70:71]
	v_cndmask_b32_sdwa v18, v1, v148, vcc dst_sel:WORD_1 dst_unused:UNUSED_PRESERVE src0_sel:WORD_1 src1_sel:WORD_1
	v_cndmask_b32_e64 v19, v1, v150, s[72:73]
	s_mov_b64 vcc, s[74:75]
	v_cndmask_b32_sdwa v19, v1, v150, vcc dst_sel:WORD_1 dst_unused:UNUSED_PRESERVE src0_sel:WORD_1 src1_sel:WORD_1
	v_mfma_f32_32x32x16_f16 a[64:79], v[114:117], v[66:69], a[64:79]
	ds_read_b128 v[86:89], v209 offset:28672
	v_cndmask_b32_e64 v20, v1, v152, s[76:77]
	s_mov_b64 vcc, s[78:79]
	v_cndmask_b32_sdwa v20, v1, v152, vcc dst_sel:WORD_1 dst_unused:UNUSED_PRESERVE src0_sel:WORD_1 src1_sel:WORD_1
	v_cndmask_b32_e64 v21, v1, v154, s[80:81]
	s_mov_b64 vcc, s[82:83]
	v_cndmask_b32_sdwa v21, v1, v154, vcc dst_sel:WORD_1 dst_unused:UNUSED_PRESERVE src0_sel:WORD_1 src1_sel:WORD_1
	v_mfma_f32_32x32x16_f16 a[176:191], v[110:113], v[66:69], a[176:191]
	v_cndmask_b32_e64 v38, v138, v156, s[52:53]
	s_mov_b64 vcc, s[54:55]
	v_cndmask_b32_sdwa v38, v138, v156, vcc dst_sel:WORD_1 dst_unused:UNUSED_PRESERVE src0_sel:WORD_1 src1_sel:WORD_1
	v_cndmask_b32_e64 v39, v138, v158, s[56:57]
	s_mov_b64 vcc, s[58:59]
	v_cndmask_b32_sdwa v39, v138, v158, vcc dst_sel:WORD_1 dst_unused:UNUSED_PRESERVE src0_sel:WORD_1 src1_sel:WORD_1
	v_mfma_f32_32x32x16_f16 a[112:127], v[114:117], v[70:73], a[112:127]
	v_cndmask_b32_e64 v40, v138, v160, s[60:61]
	s_mov_b64 vcc, s[62:63]
	v_cndmask_b32_sdwa v40, v138, v160, vcc dst_sel:WORD_1 dst_unused:UNUSED_PRESERVE src0_sel:WORD_1 src1_sel:WORD_1
	v_cndmask_b32_e64 v41, v138, v162, s[64:65]
	s_mov_b64 vcc, s[66:67]
	v_cndmask_b32_sdwa v41, v138, v162, vcc dst_sel:WORD_1 dst_unused:UNUSED_PRESERVE src0_sel:WORD_1 src1_sel:WORD_1
	v_mfma_f32_32x32x16_f16 a[160:175], v[110:113], v[70:73], a[160:175]
	v_pk_add_f16 v148, v19, v18
	v_pk_add_f16 v149, v20, v21
	v_mfma_f32_32x32x16_f16 a[128:143], v[114:117], v[78:81], a[128:143]
	v_pk_add_f16 v150, v39, v38
	v_pk_add_f16 v151, v40, v41
	v_mfma_f32_32x32x16_f16 a[144:159], v[110:113], v[78:81], a[144:159]
	v_pk_add_f16 v148, v148, v149
	v_pk_add_f16 v150, v150, v151
	v_mfma_f32_32x32x16_f16 a[80:95], v[114:117], v[102:105], a[80:95]
	v_fma_mix_f32 v134, v148, 1.0, v134 op_sel_hi:[1,0,0]
	v_fma_mix_f32 v135, v150, 1.0, v135 op_sel_hi:[1,0,0]
	v_mfma_f32_32x32x16_f16 a[96:111], v[110:113], v[102:105], a[96:111]
	v_fma_mix_f32 v134, v148, 1.0, v134 op_sel:[1,0,0] op_sel_hi:[1,0,0]
	v_fma_mix_f32 v135, v150, 1.0, v135 op_sel:[1,0,0] op_sel_hi:[1,0,0]
	s_waitcnt lgkmcnt(0)
	v_mfma_f32_32x32x16_f16 a[0:15], v[18:21], v[74:77], a[0:15]
	v_mfma_f32_32x32x16_f16 a[240:255], v[38:41], v[74:77], a[240:255]
	ds_read_b128 v[50:53], v210
	v_pk_mul_f16 v148, v46, v136
	v_pk_mul_f16 v149, v42, v137
	v_pk_mul_f16 v150, v47, v136
	v_pk_mul_f16 v151, v43, v137
	v_mfma_f32_32x32x16_f16 a[16:31], v[18:21], v[126:129], a[16:31]
	ds_read_b128 v[54:57], v210 offset:4096
	v_pk_mul_f16 v152, v48, v136
	v_pk_mul_f16 v153, v44, v137
	v_pk_mul_f16 v154, v49, v136
	v_pk_mul_f16 v155, v45, v137
	v_mfma_f32_32x32x16_f16 a[224:239], v[38:41], v[126:129], a[224:239]
	ds_read_b128 v[58:61], v210 offset:8192
	v_pk_mul_f16 v156, v46, v140
	v_pk_mul_f16 v157, v42, v139
	v_pk_mul_f16 v158, v47, v140
	v_pk_mul_f16 v159, v43, v139
	v_mfma_f32_32x32x16_f16 a[32:47], v[18:21], v[122:125], a[32:47]
	ds_read_b128 v[62:65], v210 offset:12288
	v_pk_mul_f16 v160, v48, v140
	v_pk_mul_f16 v161, v44, v139
	v_pk_mul_f16 v162, v49, v140
	v_pk_mul_f16 v163, v45, v139
	v_mfma_f32_32x32x16_f16 a[208:223], v[38:41], v[122:125], a[208:223]
	ds_read_b128 v[66:69], v210 offset:16384
	v_pk_max_f16 v148, v148, v149
	v_pk_max_f16 v150, v150, v151
	v_pk_max_f16 v152, v152, v153
	v_pk_max_f16 v154, v154, v155
	v_mfma_f32_32x32x16_f16 a[48:63], v[18:21], v[118:121], a[48:63]
	ds_read_b128 v[70:73], v210 offset:20480
	v_pk_max_f16 v156, v156, v157
	v_pk_max_f16 v158, v158, v159
	v_pk_max_f16 v160, v160, v161
	v_pk_max_f16 v162, v162, v163
	v_mfma_f32_32x32x16_f16 a[192:207], v[38:41], v[118:121], a[192:207]
	ds_read_b128 v[78:81], v210 offset:24576
	v_cndmask_b32_e64 v114, v1, v148, s[36:37]
	s_mov_b64 vcc, s[38:39]
	v_cndmask_b32_sdwa v114, v1, v148, vcc dst_sel:WORD_1 dst_unused:UNUSED_PRESERVE src0_sel:WORD_1 src1_sel:WORD_1
	v_cndmask_b32_e64 v115, v1, v150, s[40:41]
	s_mov_b64 vcc, s[42:43]
	v_cndmask_b32_sdwa v115, v1, v150, vcc dst_sel:WORD_1 dst_unused:UNUSED_PRESERVE src0_sel:WORD_1 src1_sel:WORD_1
	v_mfma_f32_32x32x16_f16 a[64:79], v[18:21], v[106:109], a[64:79]
	ds_read_b128 v[102:105], v210 offset:28672
	v_cndmask_b32_e64 v116, v1, v152, s[44:45]
	s_mov_b64 vcc, s[46:47]
	v_cndmask_b32_sdwa v116, v1, v152, vcc dst_sel:WORD_1 dst_unused:UNUSED_PRESERVE src0_sel:WORD_1 src1_sel:WORD_1
	v_cndmask_b32_e64 v117, v1, v154, s[48:49]
	s_mov_b64 vcc, s[50:51]
	v_cndmask_b32_sdwa v117, v1, v154, vcc dst_sel:WORD_1 dst_unused:UNUSED_PRESERVE src0_sel:WORD_1 src1_sel:WORD_1
	v_mfma_f32_32x32x16_f16 a[176:191], v[38:41], v[106:109], a[176:191]
	v_cndmask_b32_e64 v110, v138, v156, s[4:5]
	s_mov_b64 vcc, s[6:7]
	v_cndmask_b32_sdwa v110, v138, v156, vcc dst_sel:WORD_1 dst_unused:UNUSED_PRESERVE src0_sel:WORD_1 src1_sel:WORD_1
	v_cndmask_b32_e64 v111, v138, v158, s[8:9]
	s_mov_b64 vcc, s[10:11]
	v_cndmask_b32_sdwa v111, v138, v158, vcc dst_sel:WORD_1 dst_unused:UNUSED_PRESERVE src0_sel:WORD_1 src1_sel:WORD_1
	v_mfma_f32_32x32x16_f16 a[112:127], v[18:21], v[98:101], a[112:127]
	v_cndmask_b32_e64 v112, v138, v160, s[12:13]
	s_mov_b64 vcc, s[14:15]
	v_cndmask_b32_sdwa v112, v138, v160, vcc dst_sel:WORD_1 dst_unused:UNUSED_PRESERVE src0_sel:WORD_1 src1_sel:WORD_1
	v_cndmask_b32_e64 v113, v138, v162, s[16:17]
	s_mov_b64 vcc, s[18:19]
	v_cndmask_b32_sdwa v113, v138, v162, vcc dst_sel:WORD_1 dst_unused:UNUSED_PRESERVE src0_sel:WORD_1 src1_sel:WORD_1
	v_mfma_f32_32x32x16_f16 a[160:175], v[38:41], v[98:101], a[160:175]
	v_pk_add_f16 v148, v115, v114
	v_pk_add_f16 v149, v116, v117
	v_mfma_f32_32x32x16_f16 a[128:143], v[18:21], v[94:97], a[128:143]
	v_pk_add_f16 v150, v111, v110
	v_pk_add_f16 v151, v112, v113
	v_mfma_f32_32x32x16_f16 a[144:159], v[38:41], v[94:97], a[144:159]
	v_pk_add_f16 v148, v148, v149
	v_pk_add_f16 v150, v150, v151
	v_mfma_f32_32x32x16_f16 a[80:95], v[18:21], v[86:89], a[80:95]
	v_fma_mix_f32 v134, v148, 1.0, v134 op_sel_hi:[1,0,0]
	v_fma_mix_f32 v135, v150, 1.0, v135 op_sel_hi:[1,0,0]
	v_mfma_f32_32x32x16_f16 a[96:111], v[38:41], v[86:89], a[96:111]
	v_fma_mix_f32 v134, v148, 1.0, v134 op_sel:[1,0,0] op_sel_hi:[1,0,0]
	v_fma_mix_f32 v135, v150, 1.0, v135 op_sel:[1,0,0] op_sel_hi:[1,0,0]
	s_waitcnt lgkmcnt(0)
	v_mfma_f32_32x32x16_f16 a[0:15], v[114:117], v[50:53], a[0:15]
	v_mfma_f32_32x32x16_f16 a[240:255], v[110:113], v[50:53], a[240:255]
	v_mfma_f32_32x32x16_f16 a[16:31], v[114:117], v[54:57], a[16:31]
	v_mfma_f32_32x32x16_f16 a[224:239], v[110:113], v[54:57], a[224:239]
	v_mfma_f32_32x32x16_f16 a[32:47], v[114:117], v[58:61], a[32:47]
	v_mfma_f32_32x32x16_f16 a[208:223], v[110:113], v[58:61], a[208:223]
	v_mfma_f32_32x32x16_f16 a[48:63], v[114:117], v[62:65], a[48:63]
	v_mfma_f32_32x32x16_f16 a[192:207], v[110:113], v[62:65], a[192:207]
	v_mfma_f32_32x32x16_f16 a[64:79], v[114:117], v[66:69], a[64:79]
	v_mfma_f32_32x32x16_f16 a[176:191], v[110:113], v[66:69], a[176:191]
	v_mfma_f32_32x32x16_f16 a[112:127], v[114:117], v[70:73], a[112:127]
	v_mfma_f32_32x32x16_f16 a[160:175], v[110:113], v[70:73], a[160:175]
	v_mfma_f32_32x32x16_f16 a[128:143], v[114:117], v[78:81], a[128:143]
	v_mfma_f32_32x32x16_f16 a[144:159], v[110:113], v[78:81], a[144:159]
	v_mfma_f32_32x32x16_f16 a[80:95], v[114:117], v[102:105], a[80:95]
	v_mfma_f32_32x32x16_f16 a[96:111], v[110:113], v[102:105], a[96:111]
	v_readfirstlane_b32 s1, v0
	s_and_b32 s0, s3, 0xffffff00
	s_andn2_b32 s1, s1, 63
	s_add_i32 s4, s1, s0
	s_lshl_b32 s0, s2, 13
	s_and_b32 s6, s0, 0xe000
	s_ashr_i32 s5, s4, 31
	s_add_u32 s0, s4, s6
	s_addc_u32 s1, s5, 0
	s_lshl_b64 s[2:3], s[0:1], 9
	v_lshrrev_b32_e32 v0, 3, v132
	s_add_u32 s2, s22, s2
	v_and_b32_e32 v3, 12, v0
	s_addc_u32 s3, s23, s3
	v_lshlrev_b32_e32 v0, 9, v3
	v_mov_b32_e32 v1, 0
	v_lshl_add_u64 v[4:5], s[2:3], 0, v[0:1]
	v_lshlrev_b32_e32 v0, 4, v132
	v_and_b32_e32 v0, 0x1f0, v0
	v_lshl_add_u64 v[4:5], v[4:5], 0, v[0:1]
	v_accvgpr_read_b32 v6, a0
	v_accvgpr_read_b32 v7, a16
	v_accvgpr_read_b32 v8, a32
	v_max3_f32 v0, |v6|, |v7|, |v8|
	v_accvgpr_read_b32 v9, a48
	v_accvgpr_read_b32 v14, a64
	v_max3_f32 v0, |v0|, |v9|, |v14|
	v_accvgpr_read_b32 v15, a112
	v_accvgpr_read_b32 v16, a128
	v_max3_f32 v0, |v0|, |v15|, |v16|
	v_accvgpr_read_b32 v17, a80
	v_max3_f32 v10, |v0|, |v17|, |v17|
	v_accvgpr_read_b32 v18, a1
	v_accvgpr_read_b32 v19, a17
	v_accvgpr_read_b32 v20, a33
	v_max3_f32 v0, |v18|, |v19|, |v20|
	v_accvgpr_read_b32 v21, a49
	v_accvgpr_read_b32 v22, a65
	v_max3_f32 v0, |v0|, |v21|, |v22|
	v_accvgpr_read_b32 v23, a113
	v_accvgpr_read_b32 v24, a129
	v_max3_f32 v0, |v0|, |v23|, |v24|
	v_accvgpr_read_b32 v25, a81
	v_max3_f32 v11, |v0|, |v25|, |v25|
	v_accvgpr_read_b32 v26, a2
	v_accvgpr_read_b32 v27, a18
	v_accvgpr_read_b32 v28, a34
	v_max3_f32 v0, |v26|, |v27|, |v28|
	v_accvgpr_read_b32 v29, a50
	v_accvgpr_read_b32 v30, a66
	v_max3_f32 v0, |v0|, |v29|, |v30|
	v_accvgpr_read_b32 v31, a114
	v_accvgpr_read_b32 v32, a130
	v_max3_f32 v0, |v0|, |v31|, |v32|
	v_accvgpr_read_b32 v33, a82
	v_max3_f32 v12, |v0|, |v33|, |v33|
	v_accvgpr_read_b32 v34, a3
	v_accvgpr_read_b32 v35, a19
	v_accvgpr_read_b32 v36, a35
	v_max3_f32 v0, |v34|, |v35|, |v36|
	v_accvgpr_read_b32 v37, a51
	v_accvgpr_read_b32 v38, a67
	v_max3_f32 v0, |v0|, |v37|, |v38|
	v_accvgpr_read_b32 v39, a115
	v_accvgpr_read_b32 v40, a131
	v_max3_f32 v0, |v0|, |v39|, |v40|
	v_accvgpr_read_b32 v41, a83
	v_max3_f32 v13, |v0|, |v41|, |v41|
	v_lshlrev_b32_e32 v0, 2, v3
	s_nop 1
	v_max_f32_dpp v10, v10, v10 quad_perm:[1,0,3,2] row_mask:0xf bank_mask:0xf
	v_max_f32_dpp v11, v11, v11 quad_perm:[1,0,3,2] row_mask:0xf bank_mask:0xf
	v_max_f32_dpp v12, v12, v12 quad_perm:[1,0,3,2] row_mask:0xf bank_mask:0xf
	v_max_f32_dpp v13, v13, v13 quad_perm:[1,0,3,2] row_mask:0xf bank_mask:0xf
	v_max_f32_dpp v10, v10, v10 quad_perm:[2,3,0,1] row_mask:0xf bank_mask:0xf
	v_max_f32_dpp v11, v11, v11 quad_perm:[2,3,0,1] row_mask:0xf bank_mask:0xf
	v_max_f32_dpp v12, v12, v12 quad_perm:[2,3,0,1] row_mask:0xf bank_mask:0xf
	v_max_f32_dpp v13, v13, v13 quad_perm:[2,3,0,1] row_mask:0xf bank_mask:0xf
	v_max_f32_dpp v10, v10, v10 row_half_mirror row_mask:0xf bank_mask:0xf
	v_max_f32_dpp v11, v11, v11 row_half_mirror row_mask:0xf bank_mask:0xf
	v_max_f32_dpp v12, v12, v12 row_half_mirror row_mask:0xf bank_mask:0xf
	v_max_f32_dpp v13, v13, v13 row_half_mirror row_mask:0xf bank_mask:0xf
	v_max_f32_dpp v10, v10, v10 row_mirror row_mask:0xf bank_mask:0xf
	v_max_f32_dpp v11, v11, v11 row_mirror row_mask:0xf bank_mask:0xf
	v_max_f32_dpp v12, v12, v12 row_mirror row_mask:0xf bank_mask:0xf
	v_max_f32_dpp v13, v13, v13 row_mirror row_mask:0xf bank_mask:0xf
	s_nop 0
	ds_swizzle_b32 v232, v10 offset:swizzle(SWAP,16)
	ds_swizzle_b32 v233, v12 offset:swizzle(SWAP,16)
	ds_swizzle_b32 v234, v11 offset:swizzle(SWAP,16)
	ds_swizzle_b32 v235, v13 offset:swizzle(SWAP,16)
	s_waitcnt lgkmcnt(0)
	v_max_f32_e32 v10, v10, v232
	v_rcp_f32_e32 v42, v10
	v_cmp_lt_f32_e32 vcc, 0, v10
	s_waitcnt lgkmcnt(0)
	v_max_f32_e32 v12, v12, v233
	s_waitcnt lgkmcnt(0)
	v_max_f32_e32 v11, v11, v234
	s_lshl_b32 s2, s6, 2
	v_cndmask_b32_e32 v3, 0, v42, vcc
	v_pk_mul_f32 v[224:225], v[6:7], v[2:3] op_sel:[0,1] op_sel_hi:[1,1]
	v_pk_mul_f32 v[226:227], v[8:9], v[2:3] op_sel:[0,1] op_sel_hi:[1,1]
	v_cvt_pknorm_i16_f32 v6, v224, v225
	v_cvt_pknorm_i16_f32 v7, v226, v227
	v_pk_mul_f32 v[228:229], v[14:15], v[2:3] op_sel:[0,1] op_sel_hi:[1,1]
	v_rcp_f32_e32 v14, v11
	v_cvt_pknorm_i16_f32 v8, v228, v229
	v_pk_mul_f32 v[230:231], v[16:17], v[2:3] op_sel:[0,1] op_sel_hi:[1,1]
	v_cmp_lt_f32_e32 vcc, 0, v11
	v_cvt_pknorm_i16_f32 v9, v230, v231
	global_store_dwordx4 v[4:5], v[6:9], off sc0 sc1
	s_add_u32 s6, s24, s2
	v_cndmask_b32_e32 v3, 0, v14, vcc
	v_pk_mul_f32 v[224:225], v[18:19], v[2:3] op_sel:[0,1] op_sel_hi:[1,1]
	v_pk_mul_f32 v[226:227], v[20:21], v[2:3] op_sel:[0,1] op_sel_hi:[1,1]
	v_cvt_pknorm_i16_f32 v6, v224, v225
	v_cvt_pknorm_i16_f32 v7, v226, v227
	v_pk_mul_f32 v[228:229], v[22:23], v[2:3] op_sel:[0,1] op_sel_hi:[1,1]
	v_pk_mul_f32 v[230:231], v[24:25], v[2:3] op_sel:[0,1] op_sel_hi:[1,1]
	v_cvt_pknorm_i16_f32 v8, v228, v229
	v_cvt_pknorm_i16_f32 v9, v230, v231
	v_rcp_f32_e32 v3, v12
	s_addc_u32 s7, s25, 0
	s_lshl_b64 s[2:3], s[4:5], 2
	s_mov_b64 s[4:5], 0x200
	s_add_u32 s2, s6, s2
	v_lshl_add_u64 v[14:15], v[4:5], 0, s[4:5]
	s_mov_b32 s4, 0x38000100
	v_cmp_lt_f32_e32 vcc, 0, v12
	s_addc_u32 s3, s7, s3
	global_store_dwordx4 v[14:15], v[6:9], off sc0 sc1
	s_nop 1
	v_pk_mul_f32 v[6:7], v[10:11], s[4:5] op_sel_hi:[1,0]
	v_cndmask_b32_e32 v3, 0, v3, vcc
	global_store_dwordx2 v0, v[6:7], s[2:3]
	v_pk_mul_f32 v[224:225], v[26:27], v[2:3] op_sel:[0,1] op_sel_hi:[1,1]
	v_pk_mul_f32 v[226:227], v[28:29], v[2:3] op_sel:[0,1] op_sel_hi:[1,1]
	v_cvt_pknorm_i16_f32 v6, v224, v225
	v_cvt_pknorm_i16_f32 v7, v226, v227
	v_pk_mul_f32 v[228:229], v[30:31], v[2:3] op_sel:[0,1] op_sel_hi:[1,1]
	v_pk_mul_f32 v[230:231], v[32:33], v[2:3] op_sel:[0,1] op_sel_hi:[1,1]
	v_cvt_pknorm_i16_f32 v8, v228, v229
	s_waitcnt lgkmcnt(0)
	v_max_f32_e32 v13, v13, v235
	v_cvt_pknorm_i16_f32 v9, v230, v231
	v_rcp_f32_e32 v3, v13
	v_cmp_lt_f32_e32 vcc, 0, v13
	s_mov_b64 s[6:7], 0x400
	v_lshl_add_u64 v[10:11], v[4:5], 0, s[6:7]
	v_cndmask_b32_e32 v3, 0, v3, vcc
	global_store_dwordx4 v[10:11], v[6:9], off sc0 sc1
	v_pk_mul_f32 v[224:225], v[34:35], v[2:3] op_sel:[0,1] op_sel_hi:[1,1]
	v_pk_mul_f32 v[226:227], v[36:37], v[2:3] op_sel:[0,1] op_sel_hi:[1,1]
	v_cvt_pknorm_i16_f32 v6, v224, v225
	v_cvt_pknorm_i16_f32 v7, v226, v227
	v_pk_mul_f32 v[228:229], v[38:39], v[2:3] op_sel:[0,1] op_sel_hi:[1,1]
	v_pk_mul_f32 v[230:231], v[40:41], v[2:3] op_sel:[0,1] op_sel_hi:[1,1]
	v_cvt_pknorm_i16_f32 v8, v228, v229
	s_mov_b64 s[6:7], 0x600
	v_cvt_pknorm_i16_f32 v9, v230, v231
	v_lshl_add_u64 v[10:11], v[4:5], 0, s[6:7]
	global_store_dwordx4 v[10:11], v[6:9], off sc0 sc1
	s_nop 1
	v_pk_mul_f32 v[6:7], v[12:13], s[4:5] op_sel_hi:[1,0]
	v_lshlrev_b32_e32 v2, 2, v132
	global_store_dwordx2 v0, v[6:7], s[2:3] offset:8
	v_accvgpr_read_b32 v42, a4
	v_accvgpr_read_b32 v6, a20
	v_accvgpr_read_b32 v7, a36
	v_max3_f32 v8, |v42|, |v6|, |v7|
	v_accvgpr_read_b32 v9, a52
	v_accvgpr_read_b32 v14, a68
	v_max3_f32 v8, |v8|, |v9|, |v14|
	v_accvgpr_read_b32 v15, a116
	v_accvgpr_read_b32 v16, a132
	v_max3_f32 v8, |v8|, |v15|, |v16|
	v_accvgpr_read_b32 v10, a84
	v_accvgpr_read_b32 v43, a5
	v_accvgpr_read_b32 v17, a84
	v_max3_f32 v8, |v8|, |v17|, |v10|
	v_accvgpr_read_b32 v19, a21
	v_accvgpr_read_b32 v20, a37
	v_max3_f32 v10, |v43|, |v19|, |v20|
	v_accvgpr_read_b32 v21, a53
	v_accvgpr_read_b32 v22, a69
	v_max3_f32 v10, |v10|, |v21|, |v22|
	v_accvgpr_read_b32 v23, a117
	v_accvgpr_read_b32 v24, a133
	v_max3_f32 v10, |v10|, |v23|, |v24|
	v_accvgpr_read_b32 v44, a6
	v_accvgpr_read_b32 v25, a85
	v_max3_f32 v11, |v10|, |v25|, |v25|
	v_accvgpr_read_b32 v27, a22
	v_accvgpr_read_b32 v28, a38
	v_max3_f32 v10, |v44|, |v27|, |v28|
	v_accvgpr_read_b32 v29, a54
	v_accvgpr_read_b32 v30, a70
	v_max3_f32 v10, |v10|, |v29|, |v30|
	v_accvgpr_read_b32 v31, a118
	v_accvgpr_read_b32 v32, a134
	v_max3_f32 v10, |v10|, |v31|, |v32|
	v_accvgpr_read_b32 v45, a7
	v_accvgpr_read_b32 v33, a86
	v_max3_f32 v12, |v10|, |v33|, |v33|
	v_accvgpr_read_b32 v35, a23
	v_accvgpr_read_b32 v36, a39
	v_max3_f32 v10, |v45|, |v35|, |v36|
	v_accvgpr_read_b32 v37, a55
	v_accvgpr_read_b32 v38, a71
	v_max3_f32 v10, |v10|, |v37|, |v38|
	v_accvgpr_read_b32 v39, a119
	v_accvgpr_read_b32 v40, a135
	v_max3_f32 v10, |v10|, |v39|, |v40|
	v_accvgpr_read_b32 v41, a87
	v_max3_f32 v13, |v10|, |v41|, |v41|
	v_mov_b32_e32 v3, v42
	s_nop 1
	v_max_f32_dpp v8, v8, v8 quad_perm:[1,0,3,2] row_mask:0xf bank_mask:0xf
	v_max_f32_dpp v11, v11, v11 quad_perm:[1,0,3,2] row_mask:0xf bank_mask:0xf
	v_max_f32_dpp v12, v12, v12 quad_perm:[1,0,3,2] row_mask:0xf bank_mask:0xf
	v_max_f32_dpp v13, v13, v13 quad_perm:[1,0,3,2] row_mask:0xf bank_mask:0xf
	v_max_f32_dpp v8, v8, v8 quad_perm:[2,3,0,1] row_mask:0xf bank_mask:0xf
	v_max_f32_dpp v11, v11, v11 quad_perm:[2,3,0,1] row_mask:0xf bank_mask:0xf
	v_max_f32_dpp v12, v12, v12 quad_perm:[2,3,0,1] row_mask:0xf bank_mask:0xf
	v_max_f32_dpp v13, v13, v13 quad_perm:[2,3,0,1] row_mask:0xf bank_mask:0xf
	v_max_f32_dpp v8, v8, v8 row_half_mirror row_mask:0xf bank_mask:0xf
	v_max_f32_dpp v11, v11, v11 row_half_mirror row_mask:0xf bank_mask:0xf
	v_max_f32_dpp v12, v12, v12 row_half_mirror row_mask:0xf bank_mask:0xf
	v_max_f32_dpp v13, v13, v13 row_half_mirror row_mask:0xf bank_mask:0xf
	v_max_f32_dpp v8, v8, v8 row_mirror row_mask:0xf bank_mask:0xf
	v_max_f32_dpp v11, v11, v11 row_mirror row_mask:0xf bank_mask:0xf
	v_max_f32_dpp v12, v12, v12 row_mirror row_mask:0xf bank_mask:0xf
	v_max_f32_dpp v13, v13, v13 row_mirror row_mask:0xf bank_mask:0xf
	s_nop 0
	ds_swizzle_b32 v232, v8 offset:swizzle(SWAP,16)
	ds_swizzle_b32 v233, v11 offset:swizzle(SWAP,16)
	ds_swizzle_b32 v234, v12 offset:swizzle(SWAP,16)
	ds_swizzle_b32 v235, v13 offset:swizzle(SWAP,16)
	s_waitcnt lgkmcnt(0)
	v_max_f32_e32 v10, v8, v232
	v_rcp_f32_e32 v8, v10
	v_cmp_lt_f32_e32 vcc, 0, v10
	s_waitcnt lgkmcnt(0)
	v_max_f32_e32 v11, v11, v233
	v_mov_b32_e32 v18, v43
	s_mov_b64 s[6:7], 0x1000
	v_cndmask_b32_e32 v42, 0, v8, vcc
	v_mul_f32_e32 v3, v42, v3
	v_mul_f32_e32 v6, v42, v6
	v_cvt_pknorm_i16_f32 v6, v3, v6
	v_mul_f32_e32 v3, v42, v7
	v_mul_f32_e32 v7, v42, v9
	v_cvt_pknorm_i16_f32 v7, v3, v7
	v_pk_mul_f32 v[224:225], v[14:15], v[42:43] op_sel_hi:[1,0]
	v_pk_mul_f32 v[226:227], v[16:17], v[42:43] op_sel_hi:[1,0]
	v_cvt_pknorm_i16_f32 v8, v224, v225
	v_cvt_pknorm_i16_f32 v9, v226, v227
	v_rcp_f32_e32 v3, v11
	v_cmp_lt_f32_e32 vcc, 0, v11
	v_lshl_add_u64 v[14:15], v[4:5], 0, s[6:7]
	global_store_dwordx4 v[14:15], v[6:9], off sc0 sc1
	v_cndmask_b32_e32 v3, 0, v3, vcc
	v_pk_mul_f32 v[228:229], v[18:19], v[2:3] op_sel:[0,1] op_sel_hi:[1,1]
	v_pk_mul_f32 v[230:231], v[20:21], v[2:3] op_sel:[0,1] op_sel_hi:[1,1]
	v_cvt_pknorm_i16_f32 v6, v228, v229
	v_cvt_pknorm_i16_f32 v7, v230, v231
	v_pk_mul_f32 v[224:225], v[22:23], v[2:3] op_sel:[0,1] op_sel_hi:[1,1]
	v_pk_mul_f32 v[226:227], v[24:25], v[2:3] op_sel:[0,1] op_sel_hi:[1,1]
	v_cvt_pknorm_i16_f32 v8, v224, v225
	s_waitcnt lgkmcnt(0)
	v_max_f32_e32 v12, v12, v234
	v_cvt_pknorm_i16_f32 v9, v226, v227
	v_rcp_f32_e32 v3, v12
	s_mov_b64 s[6:7], 0x1200
	v_cmp_lt_f32_e32 vcc, 0, v12
	v_mov_b32_e32 v26, v44
	v_lshl_add_u64 v[14:15], v[4:5], 0, s[6:7]
	global_store_dwordx4 v[14:15], v[6:9], off sc0 sc1
	s_nop 1
	v_pk_mul_f32 v[6:7], v[10:11], s[4:5] op_sel_hi:[1,0]
	v_cndmask_b32_e32 v3, 0, v3, vcc
	global_store_dwordx2 v0, v[6:7], s[2:3] offset:32
	v_pk_mul_f32 v[228:229], v[26:27], v[2:3] op_sel:[0,1] op_sel_hi:[1,1]
	v_pk_mul_f32 v[230:231], v[28:29], v[2:3] op_sel:[0,1] op_sel_hi:[1,1]
	v_cvt_pknorm_i16_f32 v6, v228, v229
	v_cvt_pknorm_i16_f32 v7, v230, v231
	v_pk_mul_f32 v[224:225], v[30:31], v[2:3] op_sel:[0,1] op_sel_hi:[1,1]
	v_pk_mul_f32 v[226:227], v[32:33], v[2:3] op_sel:[0,1] op_sel_hi:[1,1]
	v_cvt_pknorm_i16_f32 v8, v224, v225
	s_waitcnt lgkmcnt(0)
	v_max_f32_e32 v13, v13, v235
	v_cvt_pknorm_i16_f32 v9, v226, v227
	v_rcp_f32_e32 v3, v13
	v_cmp_lt_f32_e32 vcc, 0, v13
	v_mov_b32_e32 v34, v45
	s_mov_b64 s[6:7], 0x1400
	v_cndmask_b32_e32 v3, 0, v3, vcc
	v_lshl_add_u64 v[10:11], v[4:5], 0, s[6:7]
	global_store_dwordx4 v[10:11], v[6:9], off sc0 sc1
	v_pk_mul_f32 v[228:229], v[34:35], v[2:3] op_sel:[0,1] op_sel_hi:[1,1]
	v_pk_mul_f32 v[230:231], v[36:37], v[2:3] op_sel:[0,1] op_sel_hi:[1,1]
	v_cvt_pknorm_i16_f32 v6, v228, v229
	v_cvt_pknorm_i16_f32 v7, v230, v231
	v_pk_mul_f32 v[224:225], v[38:39], v[2:3] op_sel:[0,1] op_sel_hi:[1,1]
	v_pk_mul_f32 v[226:227], v[40:41], v[2:3] op_sel:[0,1] op_sel_hi:[1,1]
	v_cvt_pknorm_i16_f32 v8, v224, v225
	s_mov_b64 s[6:7], 0x1600
	v_cvt_pknorm_i16_f32 v9, v226, v227
	v_lshl_add_u64 v[10:11], v[4:5], 0, s[6:7]
	global_store_dwordx4 v[10:11], v[6:9], off sc0 sc1
	s_nop 1
	v_pk_mul_f32 v[6:7], v[12:13], s[4:5] op_sel_hi:[1,0]
	v_accvgpr_read_b32 v46, a8
	v_accvgpr_read_b32 v47, a9
	v_accvgpr_read_b32 v48, a10
	v_accvgpr_read_b32 v49, a11
	v_accvgpr_read_b32 v50, a12
	v_accvgpr_read_b32 v51, a13
	v_accvgpr_read_b32 v52, a14
	v_accvgpr_read_b32 v53, a15
	global_store_dwordx2 v0, v[6:7], s[2:3] offset:40
	v_mov_b64_e32 v[42:43], v[46:47]
	v_accvgpr_read_b32 v6, a24
	v_accvgpr_read_b32 v7, a40
	v_max3_f32 v8, |v42|, |v6|, |v7|
	v_accvgpr_read_b32 v9, a56
	v_accvgpr_read_b32 v14, a72
	v_max3_f32 v8, |v8|, |v9|, |v14|
	v_accvgpr_read_b32 v15, a120
	v_accvgpr_read_b32 v16, a136
	v_max3_f32 v8, |v8|, |v15|, |v16|
	v_accvgpr_read_b32 v10, a88
	v_accvgpr_read_b32 v17, a88
	v_max3_f32 v8, |v8|, |v17|, |v10|
	v_accvgpr_read_b32 v19, a25
	v_accvgpr_read_b32 v20, a41
	v_max3_f32 v10, |v43|, |v19|, |v20|
	v_accvgpr_read_b32 v21, a57
	v_accvgpr_read_b32 v22, a73
	v_max3_f32 v10, |v10|, |v21|, |v22|
	v_accvgpr_read_b32 v23, a121
	v_accvgpr_read_b32 v24, a137
	v_max3_f32 v10, |v10|, |v23|, |v24|
	v_mov_b64_e32 v[44:45], v[48:49]
	v_accvgpr_read_b32 v25, a89
	v_max3_f32 v11, |v10|, |v25|, |v25|
	v_accvgpr_read_b32 v27, a26
	v_accvgpr_read_b32 v28, a42
	v_max3_f32 v10, |v44|, |v27|, |v28|
	v_accvgpr_read_b32 v29, a58
	v_accvgpr_read_b32 v30, a74
	v_max3_f32 v10, |v10|, |v29|, |v30|
	v_accvgpr_read_b32 v31, a122
	v_accvgpr_read_b32 v32, a138
	v_max3_f32 v10, |v10|, |v31|, |v32|
	v_accvgpr_read_b32 v33, a90
	v_max3_f32 v12, |v10|, |v33|, |v33|
	v_accvgpr_read_b32 v35, a27
	v_accvgpr_read_b32 v36, a43
	v_max3_f32 v10, |v45|, |v35|, |v36|
	v_accvgpr_read_b32 v37, a59
	v_accvgpr_read_b32 v38, a75
	v_max3_f32 v10, |v10|, |v37|, |v38|
	v_accvgpr_read_b32 v39, a123
	v_accvgpr_read_b32 v40, a139
	v_max3_f32 v10, |v10|, |v39|, |v40|
	v_accvgpr_read_b32 v41, a91
	v_max3_f32 v13, |v10|, |v41|, |v41|
	v_mov_b32_e32 v3, v42
	s_nop 1
	v_max_f32_dpp v8, v8, v8 quad_perm:[1,0,3,2] row_mask:0xf bank_mask:0xf
	v_max_f32_dpp v11, v11, v11 quad_perm:[1,0,3,2] row_mask:0xf bank_mask:0xf
	v_max_f32_dpp v12, v12, v12 quad_perm:[1,0,3,2] row_mask:0xf bank_mask:0xf
	v_max_f32_dpp v13, v13, v13 quad_perm:[1,0,3,2] row_mask:0xf bank_mask:0xf
	v_max_f32_dpp v8, v8, v8 quad_perm:[2,3,0,1] row_mask:0xf bank_mask:0xf
	v_max_f32_dpp v11, v11, v11 quad_perm:[2,3,0,1] row_mask:0xf bank_mask:0xf
	v_max_f32_dpp v12, v12, v12 quad_perm:[2,3,0,1] row_mask:0xf bank_mask:0xf
	v_max_f32_dpp v13, v13, v13 quad_perm:[2,3,0,1] row_mask:0xf bank_mask:0xf
	v_max_f32_dpp v8, v8, v8 row_half_mirror row_mask:0xf bank_mask:0xf
	v_max_f32_dpp v11, v11, v11 row_half_mirror row_mask:0xf bank_mask:0xf
	v_max_f32_dpp v12, v12, v12 row_half_mirror row_mask:0xf bank_mask:0xf
	v_max_f32_dpp v13, v13, v13 row_half_mirror row_mask:0xf bank_mask:0xf
	v_max_f32_dpp v8, v8, v8 row_mirror row_mask:0xf bank_mask:0xf
	v_max_f32_dpp v11, v11, v11 row_mirror row_mask:0xf bank_mask:0xf
	v_max_f32_dpp v12, v12, v12 row_mirror row_mask:0xf bank_mask:0xf
	v_max_f32_dpp v13, v13, v13 row_mirror row_mask:0xf bank_mask:0xf
	s_nop 0
	ds_swizzle_b32 v232, v8 offset:swizzle(SWAP,16)
	ds_swizzle_b32 v233, v11 offset:swizzle(SWAP,16)
	ds_swizzle_b32 v234, v12 offset:swizzle(SWAP,16)
	ds_swizzle_b32 v235, v13 offset:swizzle(SWAP,16)
	s_waitcnt lgkmcnt(0)
	v_max_f32_e32 v10, v8, v232
	v_rcp_f32_e32 v8, v10
	v_cmp_lt_f32_e32 vcc, 0, v10
	s_waitcnt lgkmcnt(0)
	v_max_f32_e32 v11, v11, v233
	v_mov_b32_e32 v18, v43
	s_mov_b64 s[6:7], 0x2000
	v_cndmask_b32_e32 v42, 0, v8, vcc
	v_mul_f32_e32 v3, v42, v3
	v_mul_f32_e32 v6, v42, v6
	v_cvt_pknorm_i16_f32 v6, v3, v6
	v_mul_f32_e32 v3, v42, v7
	v_mul_f32_e32 v7, v42, v9
	v_cvt_pknorm_i16_f32 v7, v3, v7
	v_pk_mul_f32 v[228:229], v[14:15], v[42:43] op_sel_hi:[1,0]
	v_pk_mul_f32 v[230:231], v[16:17], v[42:43] op_sel_hi:[1,0]
	v_cvt_pknorm_i16_f32 v8, v228, v229
	v_cvt_pknorm_i16_f32 v9, v230, v231
	v_rcp_f32_e32 v3, v11
	v_cmp_lt_f32_e32 vcc, 0, v11
	v_lshl_add_u64 v[14:15], v[4:5], 0, s[6:7]
	global_store_dwordx4 v[14:15], v[6:9], off sc0 sc1
	v_cndmask_b32_e32 v3, 0, v3, vcc
	v_pk_mul_f32 v[224:225], v[18:19], v[2:3] op_sel:[0,1] op_sel_hi:[1,1]
	v_pk_mul_f32 v[226:227], v[20:21], v[2:3] op_sel:[0,1] op_sel_hi:[1,1]
	v_cvt_pknorm_i16_f32 v6, v224, v225
	v_cvt_pknorm_i16_f32 v7, v226, v227
	v_pk_mul_f32 v[228:229], v[22:23], v[2:3] op_sel:[0,1] op_sel_hi:[1,1]
	v_pk_mul_f32 v[230:231], v[24:25], v[2:3] op_sel:[0,1] op_sel_hi:[1,1]
	v_cvt_pknorm_i16_f32 v8, v228, v229
	s_waitcnt lgkmcnt(0)
	v_max_f32_e32 v12, v12, v234
	v_cvt_pknorm_i16_f32 v9, v230, v231
	v_rcp_f32_e32 v3, v12
	s_mov_b64 s[6:7], 0x2200
	v_cmp_lt_f32_e32 vcc, 0, v12
	v_mov_b32_e32 v26, v44
	v_lshl_add_u64 v[14:15], v[4:5], 0, s[6:7]
	global_store_dwordx4 v[14:15], v[6:9], off sc0 sc1
	s_nop 1
	v_pk_mul_f32 v[6:7], v[10:11], s[4:5] op_sel_hi:[1,0]
	v_cndmask_b32_e32 v3, 0, v3, vcc
	global_store_dwordx2 v0, v[6:7], s[2:3] offset:64
	v_pk_mul_f32 v[224:225], v[26:27], v[2:3] op_sel:[0,1] op_sel_hi:[1,1]
	v_pk_mul_f32 v[226:227], v[28:29], v[2:3] op_sel:[0,1] op_sel_hi:[1,1]
	v_cvt_pknorm_i16_f32 v6, v224, v225
	v_cvt_pknorm_i16_f32 v7, v226, v227
	v_pk_mul_f32 v[228:229], v[30:31], v[2:3] op_sel:[0,1] op_sel_hi:[1,1]
	v_pk_mul_f32 v[230:231], v[32:33], v[2:3] op_sel:[0,1] op_sel_hi:[1,1]
	v_cvt_pknorm_i16_f32 v8, v228, v229
	s_waitcnt lgkmcnt(0)
	v_max_f32_e32 v13, v13, v235
	v_cvt_pknorm_i16_f32 v9, v230, v231
	v_rcp_f32_e32 v3, v13
	v_cmp_lt_f32_e32 vcc, 0, v13
	v_mov_b32_e32 v34, v45
	s_mov_b64 s[6:7], 0x2400
	v_cndmask_b32_e32 v3, 0, v3, vcc
	v_lshl_add_u64 v[10:11], v[4:5], 0, s[6:7]
	global_store_dwordx4 v[10:11], v[6:9], off sc0 sc1
	v_pk_mul_f32 v[224:225], v[34:35], v[2:3] op_sel:[0,1] op_sel_hi:[1,1]
	v_pk_mul_f32 v[226:227], v[36:37], v[2:3] op_sel:[0,1] op_sel_hi:[1,1]
	v_cvt_pknorm_i16_f32 v6, v224, v225
	v_cvt_pknorm_i16_f32 v7, v226, v227
	v_pk_mul_f32 v[228:229], v[38:39], v[2:3] op_sel:[0,1] op_sel_hi:[1,1]
	v_pk_mul_f32 v[230:231], v[40:41], v[2:3] op_sel:[0,1] op_sel_hi:[1,1]
	v_cvt_pknorm_i16_f32 v8, v228, v229
	s_mov_b64 s[6:7], 0x2600
	v_cvt_pknorm_i16_f32 v9, v230, v231
	v_lshl_add_u64 v[10:11], v[4:5], 0, s[6:7]
	global_store_dwordx4 v[10:11], v[6:9], off sc0 sc1
	s_nop 1
	v_pk_mul_f32 v[6:7], v[12:13], s[4:5] op_sel_hi:[1,0]
	v_mov_b64_e32 v[46:47], v[50:51]
	v_mov_b64_e32 v[48:49], v[52:53]
	global_store_dwordx2 v0, v[6:7], s[2:3] offset:72
	v_mov_b64_e32 v[32:33], v[46:47]
	v_accvgpr_read_b32 v6, a28
	v_accvgpr_read_b32 v7, a44
	v_max3_f32 v8, |v32|, |v6|, |v7|
	v_accvgpr_read_b32 v9, a60
	v_accvgpr_read_b32 v14, a76
	v_max3_f32 v8, |v8|, |v9|, |v14|
	v_accvgpr_read_b32 v15, a124
	v_accvgpr_read_b32 v16, a140
	v_max3_f32 v8, |v8|, |v15|, |v16|
	v_accvgpr_read_b32 v10, a92
	v_accvgpr_read_b32 v17, a92
	v_max3_f32 v8, |v8|, |v17|, |v10|
	v_accvgpr_read_b32 v19, a29
	v_accvgpr_read_b32 v20, a45
	v_max3_f32 v10, |v33|, |v19|, |v20|
	v_accvgpr_read_b32 v21, a61
	v_accvgpr_read_b32 v22, a77
	v_max3_f32 v10, |v10|, |v21|, |v22|
	v_accvgpr_read_b32 v23, a125
	v_accvgpr_read_b32 v24, a141
	v_max3_f32 v10, |v10|, |v23|, |v24|
	v_mov_b64_e32 v[34:35], v[48:49]
	v_accvgpr_read_b32 v25, a93
	v_max3_f32 v11, |v10|, |v25|, |v25|
	v_accvgpr_read_b32 v27, a30
	v_accvgpr_read_b32 v28, a46
	v_max3_f32 v10, |v34|, |v27|, |v28|
	v_accvgpr_read_b32 v29, a62
	v_accvgpr_read_b32 v30, a78
	v_max3_f32 v10, |v10|, |v29|, |v30|
	v_mov_b32_e32 v3, v32
	v_accvgpr_read_b32 v31, a126
	v_accvgpr_read_b32 v32, a142
	v_max3_f32 v10, |v10|, |v31|, |v32|
	v_mov_b32_e32 v18, v33
	v_mov_b32_e32 v26, v34
	v_accvgpr_read_b32 v33, a94
	v_max3_f32 v12, |v10|, |v33|, |v33|
	v_mov_b32_e32 v34, v35
	v_accvgpr_read_b32 v35, a31
	v_accvgpr_read_b32 v36, a47
	v_max3_f32 v10, |v34|, |v35|, |v36|
	v_accvgpr_read_b32 v37, a63
	v_accvgpr_read_b32 v38, a79
	v_max3_f32 v10, |v10|, |v37|, |v38|
	v_accvgpr_read_b32 v39, a127
	v_accvgpr_read_b32 v40, a143
	v_max3_f32 v10, |v10|, |v39|, |v40|
	v_accvgpr_read_b32 v41, a95
	v_max3_f32 v13, |v10|, |v41|, |v41|
	s_mov_b64 s[6:7], 0x3000
	s_nop 1
	v_max_f32_dpp v8, v8, v8 quad_perm:[1,0,3,2] row_mask:0xf bank_mask:0xf
	v_max_f32_dpp v11, v11, v11 quad_perm:[1,0,3,2] row_mask:0xf bank_mask:0xf
	v_max_f32_dpp v12, v12, v12 quad_perm:[1,0,3,2] row_mask:0xf bank_mask:0xf
	v_max_f32_dpp v13, v13, v13 quad_perm:[1,0,3,2] row_mask:0xf bank_mask:0xf
	v_max_f32_dpp v8, v8, v8 quad_perm:[2,3,0,1] row_mask:0xf bank_mask:0xf
	v_max_f32_dpp v11, v11, v11 quad_perm:[2,3,0,1] row_mask:0xf bank_mask:0xf
	v_max_f32_dpp v12, v12, v12 quad_perm:[2,3,0,1] row_mask:0xf bank_mask:0xf
	v_max_f32_dpp v13, v13, v13 quad_perm:[2,3,0,1] row_mask:0xf bank_mask:0xf
	v_max_f32_dpp v8, v8, v8 row_half_mirror row_mask:0xf bank_mask:0xf
	v_max_f32_dpp v11, v11, v11 row_half_mirror row_mask:0xf bank_mask:0xf
	v_max_f32_dpp v12, v12, v12 row_half_mirror row_mask:0xf bank_mask:0xf
	v_max_f32_dpp v13, v13, v13 row_half_mirror row_mask:0xf bank_mask:0xf
	v_max_f32_dpp v8, v8, v8 row_mirror row_mask:0xf bank_mask:0xf
	v_max_f32_dpp v11, v11, v11 row_mirror row_mask:0xf bank_mask:0xf
	v_max_f32_dpp v12, v12, v12 row_mirror row_mask:0xf bank_mask:0xf
	v_max_f32_dpp v13, v13, v13 row_mirror row_mask:0xf bank_mask:0xf
	s_nop 0
	ds_swizzle_b32 v232, v8 offset:swizzle(SWAP,16)
	ds_swizzle_b32 v233, v11 offset:swizzle(SWAP,16)
	ds_swizzle_b32 v234, v12 offset:swizzle(SWAP,16)
	ds_swizzle_b32 v235, v13 offset:swizzle(SWAP,16)
	s_waitcnt lgkmcnt(0)
	v_max_f32_e32 v10, v8, v232
	v_rcp_f32_e32 v8, v10
	v_cmp_lt_f32_e32 vcc, 0, v10
	s_waitcnt lgkmcnt(0)
	v_max_f32_e32 v11, v11, v233
	s_waitcnt lgkmcnt(0)
	v_max_f32_e32 v12, v12, v234
	v_cndmask_b32_e32 v42, 0, v8, vcc
	v_mul_f32_e32 v3, v42, v3
	v_mul_f32_e32 v6, v42, v6
	v_cvt_pknorm_i16_f32 v6, v3, v6
	v_mul_f32_e32 v3, v42, v7
	v_mul_f32_e32 v7, v42, v9
	v_cvt_pknorm_i16_f32 v7, v3, v7
	v_pk_mul_f32 v[224:225], v[14:15], v[42:43] op_sel_hi:[1,0]
	v_pk_mul_f32 v[226:227], v[16:17], v[42:43] op_sel_hi:[1,0]
	v_cvt_pknorm_i16_f32 v8, v224, v225
	v_cvt_pknorm_i16_f32 v9, v226, v227
	v_rcp_f32_e32 v3, v11
	v_cmp_lt_f32_e32 vcc, 0, v11
	v_lshl_add_u64 v[14:15], v[4:5], 0, s[6:7]
	global_store_dwordx4 v[14:15], v[6:9], off sc0 sc1
	s_mov_b64 s[6:7], 0x3200
	v_cndmask_b32_e32 v3, 0, v3, vcc
	v_pk_mul_f32 v[228:229], v[18:19], v[2:3] op_sel:[0,1] op_sel_hi:[1,1]
	v_pk_mul_f32 v[230:231], v[20:21], v[2:3] op_sel:[0,1] op_sel_hi:[1,1]
	v_cvt_pknorm_i16_f32 v6, v228, v229
	v_cvt_pknorm_i16_f32 v7, v230, v231
	v_pk_mul_f32 v[224:225], v[22:23], v[2:3] op_sel:[0,1] op_sel_hi:[1,1]
	v_pk_mul_f32 v[226:227], v[24:25], v[2:3] op_sel:[0,1] op_sel_hi:[1,1]
	v_cvt_pknorm_i16_f32 v8, v224, v225
	v_cvt_pknorm_i16_f32 v9, v226, v227
	v_rcp_f32_e32 v3, v12
	v_cmp_lt_f32_e32 vcc, 0, v12
	v_lshl_add_u64 v[14:15], v[4:5], 0, s[6:7]
	global_store_dwordx4 v[14:15], v[6:9], off sc0 sc1
	s_nop 1
	v_pk_mul_f32 v[6:7], v[10:11], s[4:5] op_sel_hi:[1,0]
	v_cndmask_b32_e32 v3, 0, v3, vcc
	global_store_dwordx2 v0, v[6:7], s[2:3] offset:96
	v_pk_mul_f32 v[228:229], v[26:27], v[2:3] op_sel:[0,1] op_sel_hi:[1,1]
	v_pk_mul_f32 v[230:231], v[28:29], v[2:3] op_sel:[0,1] op_sel_hi:[1,1]
	v_cvt_pknorm_i16_f32 v6, v228, v229
	v_cvt_pknorm_i16_f32 v7, v230, v231
	v_pk_mul_f32 v[224:225], v[30:31], v[2:3] op_sel:[0,1] op_sel_hi:[1,1]
	v_pk_mul_f32 v[226:227], v[32:33], v[2:3] op_sel:[0,1] op_sel_hi:[1,1]
	v_cvt_pknorm_i16_f32 v8, v224, v225
	s_waitcnt lgkmcnt(0)
	v_max_f32_e32 v13, v13, v235
	v_cvt_pknorm_i16_f32 v9, v226, v227
	v_rcp_f32_e32 v3, v13
	v_cmp_lt_f32_e32 vcc, 0, v13
	s_mov_b64 s[6:7], 0x3400
	v_lshl_add_u64 v[10:11], v[4:5], 0, s[6:7]
	v_cndmask_b32_e32 v3, 0, v3, vcc
	global_store_dwordx4 v[10:11], v[6:9], off sc0 sc1
	v_pk_mul_f32 v[228:229], v[34:35], v[2:3] op_sel:[0,1] op_sel_hi:[1,1]
	v_pk_mul_f32 v[230:231], v[36:37], v[2:3] op_sel:[0,1] op_sel_hi:[1,1]
	v_cvt_pknorm_i16_f32 v6, v228, v229
	v_cvt_pknorm_i16_f32 v7, v230, v231
	v_pk_mul_f32 v[224:225], v[38:39], v[2:3] op_sel:[0,1] op_sel_hi:[1,1]
	v_pk_mul_f32 v[226:227], v[40:41], v[2:3] op_sel:[0,1] op_sel_hi:[1,1]
	v_cvt_pknorm_i16_f32 v8, v224, v225
	s_mov_b64 s[6:7], 0x3600
	v_cvt_pknorm_i16_f32 v9, v226, v227
	v_lshl_add_u64 v[10:11], v[4:5], 0, s[6:7]
	global_store_dwordx4 v[10:11], v[6:9], off sc0 sc1
	s_nop 1
	v_pk_mul_f32 v[6:7], v[12:13], s[4:5] op_sel_hi:[1,0]
	global_store_dwordx2 v0, v[6:7], s[2:3] offset:104
	v_accvgpr_read_b32 v3, a240
	v_accvgpr_read_b32 v6, a224
	v_accvgpr_read_b32 v7, a208
	v_max3_f32 v8, |v3|, |v6|, |v7|
	v_accvgpr_read_b32 v9, a192
	v_accvgpr_read_b32 v14, a176
	v_max3_f32 v8, |v8|, |v9|, |v14|
	v_accvgpr_read_b32 v15, a160
	v_accvgpr_read_b32 v16, a144
	v_max3_f32 v8, |v8|, |v15|, |v16|
	v_accvgpr_read_b32 v10, a96
	v_accvgpr_read_b32 v17, a96
	v_max3_f32 v8, |v8|, |v17|, |v10|
	v_accvgpr_read_b32 v18, a241
	v_accvgpr_read_b32 v19, a225
	v_accvgpr_read_b32 v20, a209
	v_max3_f32 v10, |v18|, |v19|, |v20|
	v_accvgpr_read_b32 v21, a193
	v_accvgpr_read_b32 v22, a177
	v_max3_f32 v10, |v10|, |v21|, |v22|
	v_accvgpr_read_b32 v23, a161
	v_accvgpr_read_b32 v24, a145
	v_max3_f32 v10, |v10|, |v23|, |v24|
	v_accvgpr_read_b32 v25, a97
	v_max3_f32 v11, |v10|, |v25|, |v25|
	v_accvgpr_read_b32 v26, a242
	v_accvgpr_read_b32 v27, a226
	v_accvgpr_read_b32 v28, a210
	v_max3_f32 v10, |v26|, |v27|, |v28|
	v_accvgpr_read_b32 v29, a194
	v_accvgpr_read_b32 v30, a178
	v_max3_f32 v10, |v10|, |v29|, |v30|
	v_accvgpr_read_b32 v31, a162
	v_accvgpr_read_b32 v32, a146
	v_max3_f32 v10, |v10|, |v31|, |v32|
	v_accvgpr_read_b32 v33, a98
	v_max3_f32 v12, |v10|, |v33|, |v33|
	v_accvgpr_read_b32 v34, a243
	v_accvgpr_read_b32 v35, a227
	v_accvgpr_read_b32 v36, a211
	v_max3_f32 v10, |v34|, |v35|, |v36|
	v_accvgpr_read_b32 v37, a195
	v_accvgpr_read_b32 v38, a179
	v_max3_f32 v10, |v10|, |v37|, |v38|
	v_accvgpr_read_b32 v39, a163
	v_accvgpr_read_b32 v40, a147
	v_max3_f32 v10, |v10|, |v39|, |v40|
	v_accvgpr_read_b32 v41, a99
	v_max3_f32 v13, |v10|, |v41|, |v41|
	s_mov_b64 s[6:7], 0x4000
	s_nop 1
	v_max_f32_dpp v8, v8, v8 quad_perm:[1,0,3,2] row_mask:0xf bank_mask:0xf
	v_max_f32_dpp v11, v11, v11 quad_perm:[1,0,3,2] row_mask:0xf bank_mask:0xf
	v_max_f32_dpp v12, v12, v12 quad_perm:[1,0,3,2] row_mask:0xf bank_mask:0xf
	v_max_f32_dpp v13, v13, v13 quad_perm:[1,0,3,2] row_mask:0xf bank_mask:0xf
	v_max_f32_dpp v8, v8, v8 quad_perm:[2,3,0,1] row_mask:0xf bank_mask:0xf
	v_max_f32_dpp v11, v11, v11 quad_perm:[2,3,0,1] row_mask:0xf bank_mask:0xf
	v_max_f32_dpp v12, v12, v12 quad_perm:[2,3,0,1] row_mask:0xf bank_mask:0xf
	v_max_f32_dpp v13, v13, v13 quad_perm:[2,3,0,1] row_mask:0xf bank_mask:0xf
	v_max_f32_dpp v8, v8, v8 row_half_mirror row_mask:0xf bank_mask:0xf
	v_max_f32_dpp v11, v11, v11 row_half_mirror row_mask:0xf bank_mask:0xf
	v_max_f32_dpp v12, v12, v12 row_half_mirror row_mask:0xf bank_mask:0xf
	v_max_f32_dpp v13, v13, v13 row_half_mirror row_mask:0xf bank_mask:0xf
	v_max_f32_dpp v8, v8, v8 row_mirror row_mask:0xf bank_mask:0xf
	v_max_f32_dpp v11, v11, v11 row_mirror row_mask:0xf bank_mask:0xf
	v_max_f32_dpp v12, v12, v12 row_mirror row_mask:0xf bank_mask:0xf
	v_max_f32_dpp v13, v13, v13 row_mirror row_mask:0xf bank_mask:0xf
	s_nop 0
	ds_swizzle_b32 v232, v8 offset:swizzle(SWAP,16)
	ds_swizzle_b32 v233, v11 offset:swizzle(SWAP,16)
	ds_swizzle_b32 v234, v12 offset:swizzle(SWAP,16)
	ds_swizzle_b32 v235, v13 offset:swizzle(SWAP,16)
	s_waitcnt lgkmcnt(0)
	v_max_f32_e32 v10, v8, v232
	v_rcp_f32_e32 v8, v10
	v_cmp_lt_f32_e32 vcc, 0, v10
	s_waitcnt lgkmcnt(0)
	v_max_f32_e32 v11, v11, v233
	s_waitcnt lgkmcnt(0)
	v_max_f32_e32 v12, v12, v234
	v_cndmask_b32_e32 v42, 0, v8, vcc
	v_mul_f32_e32 v3, v42, v3
	v_mul_f32_e32 v6, v42, v6
	v_cvt_pknorm_i16_f32 v6, v3, v6
	v_mul_f32_e32 v3, v42, v7
	v_mul_f32_e32 v7, v42, v9
	v_cvt_pknorm_i16_f32 v7, v3, v7
	v_pk_mul_f32 v[228:229], v[14:15], v[42:43] op_sel_hi:[1,0]
	v_pk_mul_f32 v[230:231], v[16:17], v[42:43] op_sel_hi:[1,0]
	v_cvt_pknorm_i16_f32 v8, v228, v229
	v_cvt_pknorm_i16_f32 v9, v230, v231
	v_rcp_f32_e32 v3, v11
	v_cmp_lt_f32_e32 vcc, 0, v11
	v_lshl_add_u64 v[14:15], v[4:5], 0, s[6:7]
	global_store_dwordx4 v[14:15], v[6:9], off sc0 sc1
	s_mov_b64 s[6:7], 0x4200
	v_cndmask_b32_e32 v3, 0, v3, vcc
	v_pk_mul_f32 v[224:225], v[18:19], v[2:3] op_sel:[0,1] op_sel_hi:[1,1]
	v_pk_mul_f32 v[226:227], v[20:21], v[2:3] op_sel:[0,1] op_sel_hi:[1,1]
	v_cvt_pknorm_i16_f32 v6, v224, v225
	v_cvt_pknorm_i16_f32 v7, v226, v227
	v_pk_mul_f32 v[228:229], v[22:23], v[2:3] op_sel:[0,1] op_sel_hi:[1,1]
	v_pk_mul_f32 v[230:231], v[24:25], v[2:3] op_sel:[0,1] op_sel_hi:[1,1]
	v_cvt_pknorm_i16_f32 v8, v228, v229
	v_cvt_pknorm_i16_f32 v9, v230, v231
	v_rcp_f32_e32 v3, v12
	v_cmp_lt_f32_e32 vcc, 0, v12
	v_lshl_add_u64 v[14:15], v[4:5], 0, s[6:7]
	global_store_dwordx4 v[14:15], v[6:9], off sc0 sc1
	s_nop 1
	v_pk_mul_f32 v[6:7], v[10:11], s[4:5] op_sel_hi:[1,0]
	v_cndmask_b32_e32 v3, 0, v3, vcc
	global_store_dwordx2 v0, v[6:7], s[2:3] offset:128
	v_pk_mul_f32 v[224:225], v[26:27], v[2:3] op_sel:[0,1] op_sel_hi:[1,1]
	v_pk_mul_f32 v[226:227], v[28:29], v[2:3] op_sel:[0,1] op_sel_hi:[1,1]
	v_cvt_pknorm_i16_f32 v6, v224, v225
	v_cvt_pknorm_i16_f32 v7, v226, v227
	v_pk_mul_f32 v[228:229], v[30:31], v[2:3] op_sel:[0,1] op_sel_hi:[1,1]
	v_pk_mul_f32 v[230:231], v[32:33], v[2:3] op_sel:[0,1] op_sel_hi:[1,1]
	v_cvt_pknorm_i16_f32 v8, v228, v229
	s_waitcnt lgkmcnt(0)
	v_max_f32_e32 v13, v13, v235
	v_cvt_pknorm_i16_f32 v9, v230, v231
	v_rcp_f32_e32 v3, v13
	v_cmp_lt_f32_e32 vcc, 0, v13
	s_mov_b64 s[6:7], 0x4400
	v_lshl_add_u64 v[10:11], v[4:5], 0, s[6:7]
	v_cndmask_b32_e32 v3, 0, v3, vcc
	global_store_dwordx4 v[10:11], v[6:9], off sc0 sc1
	v_pk_mul_f32 v[224:225], v[34:35], v[2:3] op_sel:[0,1] op_sel_hi:[1,1]
	v_pk_mul_f32 v[226:227], v[36:37], v[2:3] op_sel:[0,1] op_sel_hi:[1,1]
	v_cvt_pknorm_i16_f32 v6, v224, v225
	v_cvt_pknorm_i16_f32 v7, v226, v227
	v_pk_mul_f32 v[228:229], v[38:39], v[2:3] op_sel:[0,1] op_sel_hi:[1,1]
	v_pk_mul_f32 v[230:231], v[40:41], v[2:3] op_sel:[0,1] op_sel_hi:[1,1]
	v_cvt_pknorm_i16_f32 v8, v228, v229
	s_mov_b64 s[6:7], 0x4600
	v_cvt_pknorm_i16_f32 v9, v230, v231
	v_lshl_add_u64 v[10:11], v[4:5], 0, s[6:7]
	global_store_dwordx4 v[10:11], v[6:9], off sc0 sc1
	s_nop 1
	v_pk_mul_f32 v[6:7], v[12:13], s[4:5] op_sel_hi:[1,0]
	global_store_dwordx2 v0, v[6:7], s[2:3] offset:136
	v_accvgpr_read_b32 v3, a244
	v_accvgpr_read_b32 v6, a228
	v_accvgpr_read_b32 v7, a212
	v_max3_f32 v8, |v3|, |v6|, |v7|
	v_accvgpr_read_b32 v9, a196
	v_accvgpr_read_b32 v14, a180
	v_max3_f32 v8, |v8|, |v9|, |v14|
	v_accvgpr_read_b32 v15, a164
	v_accvgpr_read_b32 v16, a148
	v_max3_f32 v8, |v8|, |v15|, |v16|
	v_accvgpr_read_b32 v10, a100
	v_accvgpr_read_b32 v17, a100
	v_max3_f32 v8, |v8|, |v17|, |v10|
	v_accvgpr_read_b32 v18, a245
	v_accvgpr_read_b32 v19, a229
	v_accvgpr_read_b32 v20, a213
	v_max3_f32 v10, |v18|, |v19|, |v20|
	v_accvgpr_read_b32 v21, a197
	v_accvgpr_read_b32 v22, a181
	v_max3_f32 v10, |v10|, |v21|, |v22|
	v_accvgpr_read_b32 v23, a165
	v_accvgpr_read_b32 v24, a149
	v_max3_f32 v10, |v10|, |v23|, |v24|
	v_accvgpr_read_b32 v25, a101
	v_max3_f32 v11, |v10|, |v25|, |v25|
	v_accvgpr_read_b32 v26, a246
	v_accvgpr_read_b32 v27, a230
	v_accvgpr_read_b32 v28, a214
	v_max3_f32 v10, |v26|, |v27|, |v28|
	v_accvgpr_read_b32 v29, a198
	v_accvgpr_read_b32 v30, a182
	v_max3_f32 v10, |v10|, |v29|, |v30|
	v_accvgpr_read_b32 v31, a166
	v_accvgpr_read_b32 v32, a150
	v_max3_f32 v10, |v10|, |v31|, |v32|
	v_accvgpr_read_b32 v33, a102
	v_max3_f32 v12, |v10|, |v33|, |v33|
	v_accvgpr_read_b32 v34, a247
	v_accvgpr_read_b32 v35, a231
	v_accvgpr_read_b32 v36, a215
	v_max3_f32 v10, |v34|, |v35|, |v36|
	v_accvgpr_read_b32 v37, a199
	v_accvgpr_read_b32 v38, a183
	v_max3_f32 v10, |v10|, |v37|, |v38|
	v_accvgpr_read_b32 v39, a167
	v_accvgpr_read_b32 v40, a151
	v_max3_f32 v10, |v10|, |v39|, |v40|
	v_accvgpr_read_b32 v41, a103
	v_max3_f32 v13, |v10|, |v41|, |v41|
	s_mov_b64 s[6:7], 0x5000
	s_nop 1
	v_max_f32_dpp v8, v8, v8 quad_perm:[1,0,3,2] row_mask:0xf bank_mask:0xf
	v_max_f32_dpp v11, v11, v11 quad_perm:[1,0,3,2] row_mask:0xf bank_mask:0xf
	v_max_f32_dpp v12, v12, v12 quad_perm:[1,0,3,2] row_mask:0xf bank_mask:0xf
	v_max_f32_dpp v13, v13, v13 quad_perm:[1,0,3,2] row_mask:0xf bank_mask:0xf
	v_max_f32_dpp v8, v8, v8 quad_perm:[2,3,0,1] row_mask:0xf bank_mask:0xf
	v_max_f32_dpp v11, v11, v11 quad_perm:[2,3,0,1] row_mask:0xf bank_mask:0xf
	v_max_f32_dpp v12, v12, v12 quad_perm:[2,3,0,1] row_mask:0xf bank_mask:0xf
	v_max_f32_dpp v13, v13, v13 quad_perm:[2,3,0,1] row_mask:0xf bank_mask:0xf
	v_max_f32_dpp v8, v8, v8 row_half_mirror row_mask:0xf bank_mask:0xf
	v_max_f32_dpp v11, v11, v11 row_half_mirror row_mask:0xf bank_mask:0xf
	v_max_f32_dpp v12, v12, v12 row_half_mirror row_mask:0xf bank_mask:0xf
	v_max_f32_dpp v13, v13, v13 row_half_mirror row_mask:0xf bank_mask:0xf
	v_max_f32_dpp v8, v8, v8 row_mirror row_mask:0xf bank_mask:0xf
	v_max_f32_dpp v11, v11, v11 row_mirror row_mask:0xf bank_mask:0xf
	v_max_f32_dpp v12, v12, v12 row_mirror row_mask:0xf bank_mask:0xf
	v_max_f32_dpp v13, v13, v13 row_mirror row_mask:0xf bank_mask:0xf
	s_nop 0
	ds_swizzle_b32 v232, v8 offset:swizzle(SWAP,16)
	ds_swizzle_b32 v233, v11 offset:swizzle(SWAP,16)
	ds_swizzle_b32 v234, v12 offset:swizzle(SWAP,16)
	ds_swizzle_b32 v235, v13 offset:swizzle(SWAP,16)
	s_waitcnt lgkmcnt(0)
	v_max_f32_e32 v10, v8, v232
	v_rcp_f32_e32 v8, v10
	v_cmp_lt_f32_e32 vcc, 0, v10
	s_waitcnt lgkmcnt(0)
	v_max_f32_e32 v11, v11, v233
	s_waitcnt lgkmcnt(0)
	v_max_f32_e32 v12, v12, v234
	v_cndmask_b32_e32 v42, 0, v8, vcc
	v_mul_f32_e32 v3, v42, v3
	v_mul_f32_e32 v6, v42, v6
	v_cvt_pknorm_i16_f32 v6, v3, v6
	v_mul_f32_e32 v3, v42, v7
	v_mul_f32_e32 v7, v42, v9
	v_cvt_pknorm_i16_f32 v7, v3, v7
	v_pk_mul_f32 v[224:225], v[14:15], v[42:43] op_sel_hi:[1,0]
	v_pk_mul_f32 v[226:227], v[16:17], v[42:43] op_sel_hi:[1,0]
	v_cvt_pknorm_i16_f32 v8, v224, v225
	v_cvt_pknorm_i16_f32 v9, v226, v227
	v_rcp_f32_e32 v3, v11
	v_cmp_lt_f32_e32 vcc, 0, v11
	v_lshl_add_u64 v[14:15], v[4:5], 0, s[6:7]
	global_store_dwordx4 v[14:15], v[6:9], off sc0 sc1
	s_mov_b64 s[6:7], 0x5200
	v_cndmask_b32_e32 v3, 0, v3, vcc
	v_pk_mul_f32 v[228:229], v[18:19], v[2:3] op_sel:[0,1] op_sel_hi:[1,1]
	v_pk_mul_f32 v[230:231], v[20:21], v[2:3] op_sel:[0,1] op_sel_hi:[1,1]
	v_cvt_pknorm_i16_f32 v6, v228, v229
	v_cvt_pknorm_i16_f32 v7, v230, v231
	v_pk_mul_f32 v[224:225], v[22:23], v[2:3] op_sel:[0,1] op_sel_hi:[1,1]
	v_pk_mul_f32 v[226:227], v[24:25], v[2:3] op_sel:[0,1] op_sel_hi:[1,1]
	v_cvt_pknorm_i16_f32 v8, v224, v225
	v_cvt_pknorm_i16_f32 v9, v226, v227
	v_rcp_f32_e32 v3, v12
	v_cmp_lt_f32_e32 vcc, 0, v12
	v_lshl_add_u64 v[14:15], v[4:5], 0, s[6:7]
	global_store_dwordx4 v[14:15], v[6:9], off sc0 sc1
	s_nop 1
	v_pk_mul_f32 v[6:7], v[10:11], s[4:5] op_sel_hi:[1,0]
	v_cndmask_b32_e32 v3, 0, v3, vcc
	global_store_dwordx2 v0, v[6:7], s[2:3] offset:160
	v_pk_mul_f32 v[228:229], v[26:27], v[2:3] op_sel:[0,1] op_sel_hi:[1,1]
	v_pk_mul_f32 v[230:231], v[28:29], v[2:3] op_sel:[0,1] op_sel_hi:[1,1]
	v_cvt_pknorm_i16_f32 v6, v228, v229
	v_cvt_pknorm_i16_f32 v7, v230, v231
	v_pk_mul_f32 v[224:225], v[30:31], v[2:3] op_sel:[0,1] op_sel_hi:[1,1]
	v_pk_mul_f32 v[226:227], v[32:33], v[2:3] op_sel:[0,1] op_sel_hi:[1,1]
	v_cvt_pknorm_i16_f32 v8, v224, v225
	s_waitcnt lgkmcnt(0)
	v_max_f32_e32 v13, v13, v235
	v_cvt_pknorm_i16_f32 v9, v226, v227
	v_rcp_f32_e32 v3, v13
	v_cmp_lt_f32_e32 vcc, 0, v13
	s_mov_b64 s[6:7], 0x5400
	v_lshl_add_u64 v[10:11], v[4:5], 0, s[6:7]
	v_cndmask_b32_e32 v3, 0, v3, vcc
	global_store_dwordx4 v[10:11], v[6:9], off sc0 sc1
	v_pk_mul_f32 v[228:229], v[34:35], v[2:3] op_sel:[0,1] op_sel_hi:[1,1]
	v_pk_mul_f32 v[230:231], v[36:37], v[2:3] op_sel:[0,1] op_sel_hi:[1,1]
	v_cvt_pknorm_i16_f32 v6, v228, v229
	v_cvt_pknorm_i16_f32 v7, v230, v231
	v_pk_mul_f32 v[224:225], v[38:39], v[2:3] op_sel:[0,1] op_sel_hi:[1,1]
	v_pk_mul_f32 v[226:227], v[40:41], v[2:3] op_sel:[0,1] op_sel_hi:[1,1]
	v_cvt_pknorm_i16_f32 v8, v224, v225
	s_mov_b64 s[6:7], 0x5600
	v_cvt_pknorm_i16_f32 v9, v226, v227
	v_lshl_add_u64 v[10:11], v[4:5], 0, s[6:7]
	global_store_dwordx4 v[10:11], v[6:9], off sc0 sc1
	s_nop 1
	v_pk_mul_f32 v[6:7], v[12:13], s[4:5] op_sel_hi:[1,0]
	global_store_dwordx2 v0, v[6:7], s[2:3] offset:168
	v_accvgpr_read_b32 v3, a248
	v_accvgpr_read_b32 v6, a232
	v_accvgpr_read_b32 v7, a216
	v_max3_f32 v8, |v3|, |v6|, |v7|
	v_accvgpr_read_b32 v9, a200
	v_accvgpr_read_b32 v14, a184
	v_max3_f32 v8, |v8|, |v9|, |v14|
	v_accvgpr_read_b32 v15, a168
	v_accvgpr_read_b32 v16, a152
	v_max3_f32 v8, |v8|, |v15|, |v16|
	v_accvgpr_read_b32 v10, a104
	v_accvgpr_read_b32 v17, a104
	v_max3_f32 v8, |v8|, |v17|, |v10|
	v_accvgpr_read_b32 v18, a249
	v_accvgpr_read_b32 v19, a233
	v_accvgpr_read_b32 v20, a217
	v_max3_f32 v10, |v18|, |v19|, |v20|
	v_accvgpr_read_b32 v21, a201
	v_accvgpr_read_b32 v22, a185
	v_max3_f32 v10, |v10|, |v21|, |v22|
	v_accvgpr_read_b32 v23, a169
	v_accvgpr_read_b32 v24, a153
	v_max3_f32 v10, |v10|, |v23|, |v24|
	v_accvgpr_read_b32 v25, a105
	v_max3_f32 v11, |v10|, |v25|, |v25|
	v_accvgpr_read_b32 v26, a250
	v_accvgpr_read_b32 v27, a234
	v_accvgpr_read_b32 v28, a218
	v_max3_f32 v10, |v26|, |v27|, |v28|
	v_accvgpr_read_b32 v29, a202
	v_accvgpr_read_b32 v30, a186
	v_max3_f32 v10, |v10|, |v29|, |v30|
	v_accvgpr_read_b32 v31, a170
	v_accvgpr_read_b32 v32, a154
	v_max3_f32 v10, |v10|, |v31|, |v32|
	v_accvgpr_read_b32 v33, a106
	v_max3_f32 v12, |v10|, |v33|, |v33|
	v_accvgpr_read_b32 v34, a251
	v_accvgpr_read_b32 v35, a235
	v_accvgpr_read_b32 v36, a219
	v_max3_f32 v10, |v34|, |v35|, |v36|
	v_accvgpr_read_b32 v37, a203
	v_accvgpr_read_b32 v38, a187
	v_max3_f32 v10, |v10|, |v37|, |v38|
	v_accvgpr_read_b32 v39, a171
	v_accvgpr_read_b32 v40, a155
	v_max3_f32 v10, |v10|, |v39|, |v40|
	v_accvgpr_read_b32 v41, a107
	v_max3_f32 v13, |v10|, |v41|, |v41|
	s_mov_b64 s[6:7], 0x6000
	s_nop 1
	v_max_f32_dpp v8, v8, v8 quad_perm:[1,0,3,2] row_mask:0xf bank_mask:0xf
	v_max_f32_dpp v11, v11, v11 quad_perm:[1,0,3,2] row_mask:0xf bank_mask:0xf
	v_max_f32_dpp v12, v12, v12 quad_perm:[1,0,3,2] row_mask:0xf bank_mask:0xf
	v_max_f32_dpp v13, v13, v13 quad_perm:[1,0,3,2] row_mask:0xf bank_mask:0xf
	v_max_f32_dpp v8, v8, v8 quad_perm:[2,3,0,1] row_mask:0xf bank_mask:0xf
	v_max_f32_dpp v11, v11, v11 quad_perm:[2,3,0,1] row_mask:0xf bank_mask:0xf
	v_max_f32_dpp v12, v12, v12 quad_perm:[2,3,0,1] row_mask:0xf bank_mask:0xf
	v_max_f32_dpp v13, v13, v13 quad_perm:[2,3,0,1] row_mask:0xf bank_mask:0xf
	v_max_f32_dpp v8, v8, v8 row_half_mirror row_mask:0xf bank_mask:0xf
	v_max_f32_dpp v11, v11, v11 row_half_mirror row_mask:0xf bank_mask:0xf
	v_max_f32_dpp v12, v12, v12 row_half_mirror row_mask:0xf bank_mask:0xf
	v_max_f32_dpp v13, v13, v13 row_half_mirror row_mask:0xf bank_mask:0xf
	v_max_f32_dpp v8, v8, v8 row_mirror row_mask:0xf bank_mask:0xf
	v_max_f32_dpp v11, v11, v11 row_mirror row_mask:0xf bank_mask:0xf
	v_max_f32_dpp v12, v12, v12 row_mirror row_mask:0xf bank_mask:0xf
	v_max_f32_dpp v13, v13, v13 row_mirror row_mask:0xf bank_mask:0xf
	s_nop 0
	ds_swizzle_b32 v232, v8 offset:swizzle(SWAP,16)
	ds_swizzle_b32 v233, v11 offset:swizzle(SWAP,16)
	ds_swizzle_b32 v234, v12 offset:swizzle(SWAP,16)
	ds_swizzle_b32 v235, v13 offset:swizzle(SWAP,16)
	s_waitcnt lgkmcnt(0)
	v_max_f32_e32 v10, v8, v232
	v_rcp_f32_e32 v8, v10
	v_cmp_lt_f32_e32 vcc, 0, v10
	s_waitcnt lgkmcnt(0)
	v_max_f32_e32 v11, v11, v233
	s_waitcnt lgkmcnt(0)
	v_max_f32_e32 v12, v12, v234
	v_cndmask_b32_e32 v42, 0, v8, vcc
	v_mul_f32_e32 v3, v42, v3
	v_mul_f32_e32 v6, v42, v6
	v_cvt_pknorm_i16_f32 v6, v3, v6
	v_mul_f32_e32 v3, v42, v7
	v_mul_f32_e32 v7, v42, v9
	v_cvt_pknorm_i16_f32 v7, v3, v7
	v_pk_mul_f32 v[228:229], v[14:15], v[42:43] op_sel_hi:[1,0]
	v_pk_mul_f32 v[230:231], v[16:17], v[42:43] op_sel_hi:[1,0]
	v_cvt_pknorm_i16_f32 v8, v228, v229
	v_cvt_pknorm_i16_f32 v9, v230, v231
	v_rcp_f32_e32 v3, v11
	v_cmp_lt_f32_e32 vcc, 0, v11
	v_lshl_add_u64 v[14:15], v[4:5], 0, s[6:7]
	global_store_dwordx4 v[14:15], v[6:9], off sc0 sc1
	s_mov_b64 s[6:7], 0x6200
	v_cndmask_b32_e32 v3, 0, v3, vcc
	v_pk_mul_f32 v[224:225], v[18:19], v[2:3] op_sel:[0,1] op_sel_hi:[1,1]
	v_pk_mul_f32 v[226:227], v[20:21], v[2:3] op_sel:[0,1] op_sel_hi:[1,1]
	v_cvt_pknorm_i16_f32 v6, v224, v225
	v_cvt_pknorm_i16_f32 v7, v226, v227
	v_pk_mul_f32 v[228:229], v[22:23], v[2:3] op_sel:[0,1] op_sel_hi:[1,1]
	v_pk_mul_f32 v[230:231], v[24:25], v[2:3] op_sel:[0,1] op_sel_hi:[1,1]
	v_cvt_pknorm_i16_f32 v8, v228, v229
	v_cvt_pknorm_i16_f32 v9, v230, v231
	v_rcp_f32_e32 v3, v12
	v_cmp_lt_f32_e32 vcc, 0, v12
	v_lshl_add_u64 v[14:15], v[4:5], 0, s[6:7]
	global_store_dwordx4 v[14:15], v[6:9], off sc0 sc1
	s_nop 1
	v_pk_mul_f32 v[6:7], v[10:11], s[4:5] op_sel_hi:[1,0]
	v_cndmask_b32_e32 v3, 0, v3, vcc
	global_store_dwordx2 v0, v[6:7], s[2:3] offset:192
	v_pk_mul_f32 v[224:225], v[26:27], v[2:3] op_sel:[0,1] op_sel_hi:[1,1]
	v_pk_mul_f32 v[226:227], v[28:29], v[2:3] op_sel:[0,1] op_sel_hi:[1,1]
	v_cvt_pknorm_i16_f32 v6, v224, v225
	v_cvt_pknorm_i16_f32 v7, v226, v227
	v_pk_mul_f32 v[228:229], v[30:31], v[2:3] op_sel:[0,1] op_sel_hi:[1,1]
	v_pk_mul_f32 v[230:231], v[32:33], v[2:3] op_sel:[0,1] op_sel_hi:[1,1]
	v_cvt_pknorm_i16_f32 v8, v228, v229
	s_waitcnt lgkmcnt(0)
	v_max_f32_e32 v13, v13, v235
	v_cvt_pknorm_i16_f32 v9, v230, v231
	v_rcp_f32_e32 v3, v13
	v_cmp_lt_f32_e32 vcc, 0, v13
	s_mov_b64 s[6:7], 0x6400
	v_lshl_add_u64 v[10:11], v[4:5], 0, s[6:7]
	v_cndmask_b32_e32 v3, 0, v3, vcc
	global_store_dwordx4 v[10:11], v[6:9], off sc0 sc1
	v_pk_mul_f32 v[224:225], v[34:35], v[2:3] op_sel:[0,1] op_sel_hi:[1,1]
	v_pk_mul_f32 v[226:227], v[36:37], v[2:3] op_sel:[0,1] op_sel_hi:[1,1]
	v_cvt_pknorm_i16_f32 v6, v224, v225
	v_cvt_pknorm_i16_f32 v7, v226, v227
	v_pk_mul_f32 v[228:229], v[38:39], v[2:3] op_sel:[0,1] op_sel_hi:[1,1]
	v_pk_mul_f32 v[230:231], v[40:41], v[2:3] op_sel:[0,1] op_sel_hi:[1,1]
	v_cvt_pknorm_i16_f32 v8, v228, v229
	s_mov_b64 s[6:7], 0x6600
	v_cvt_pknorm_i16_f32 v9, v230, v231
	v_lshl_add_u64 v[10:11], v[4:5], 0, s[6:7]
	global_store_dwordx4 v[10:11], v[6:9], off sc0 sc1
	s_nop 1
	v_pk_mul_f32 v[6:7], v[12:13], s[4:5] op_sel_hi:[1,0]
	global_store_dwordx2 v0, v[6:7], s[2:3] offset:200
	v_accvgpr_read_b32 v3, a252
	v_accvgpr_read_b32 v6, a236
	v_accvgpr_read_b32 v7, a220
	v_max3_f32 v8, |v3|, |v6|, |v7|
	v_accvgpr_read_b32 v9, a204
	v_accvgpr_read_b32 v14, a188
	v_max3_f32 v8, |v8|, |v9|, |v14|
	v_accvgpr_read_b32 v15, a172
	v_accvgpr_read_b32 v16, a156
	v_max3_f32 v8, |v8|, |v15|, |v16|
	v_accvgpr_read_b32 v10, a108
	v_accvgpr_read_b32 v17, a108
	v_max3_f32 v8, |v8|, |v17|, |v10|
	v_accvgpr_read_b32 v18, a253
	v_accvgpr_read_b32 v19, a237
	v_accvgpr_read_b32 v20, a221
	v_max3_f32 v10, |v18|, |v19|, |v20|
	v_accvgpr_read_b32 v21, a205
	v_accvgpr_read_b32 v22, a189
	v_max3_f32 v10, |v10|, |v21|, |v22|
	v_accvgpr_read_b32 v23, a173
	v_accvgpr_read_b32 v24, a157
	v_max3_f32 v10, |v10|, |v23|, |v24|
	v_accvgpr_read_b32 v25, a109
	v_max3_f32 v11, |v10|, |v25|, |v25|
	v_accvgpr_read_b32 v26, a254
	v_accvgpr_read_b32 v27, a238
	v_accvgpr_read_b32 v28, a222
	v_max3_f32 v10, |v26|, |v27|, |v28|
	v_accvgpr_read_b32 v29, a206
	v_accvgpr_read_b32 v30, a190
	v_max3_f32 v10, |v10|, |v29|, |v30|
	v_accvgpr_read_b32 v31, a174
	v_accvgpr_read_b32 v32, a158
	v_max3_f32 v10, |v10|, |v31|, |v32|
	v_accvgpr_read_b32 v33, a110
	v_max3_f32 v12, |v10|, |v33|, |v33|
	v_accvgpr_read_b32 v34, a255
	v_accvgpr_read_b32 v35, a239
	v_accvgpr_read_b32 v36, a223
	v_max3_f32 v10, |v34|, |v35|, |v36|
	v_accvgpr_read_b32 v37, a207
	v_accvgpr_read_b32 v38, a191
	v_max3_f32 v10, |v10|, |v37|, |v38|
	v_accvgpr_read_b32 v39, a175
	v_accvgpr_read_b32 v40, a159
	v_max3_f32 v10, |v10|, |v39|, |v40|
	v_accvgpr_read_b32 v41, a111
	v_max3_f32 v13, |v10|, |v41|, |v41|
	s_mov_b64 s[6:7], 0x7000
	s_nop 1
	v_max_f32_dpp v8, v8, v8 quad_perm:[1,0,3,2] row_mask:0xf bank_mask:0xf
	v_max_f32_dpp v11, v11, v11 quad_perm:[1,0,3,2] row_mask:0xf bank_mask:0xf
	v_max_f32_dpp v12, v12, v12 quad_perm:[1,0,3,2] row_mask:0xf bank_mask:0xf
	v_max_f32_dpp v13, v13, v13 quad_perm:[1,0,3,2] row_mask:0xf bank_mask:0xf
	v_max_f32_dpp v8, v8, v8 quad_perm:[2,3,0,1] row_mask:0xf bank_mask:0xf
	v_max_f32_dpp v11, v11, v11 quad_perm:[2,3,0,1] row_mask:0xf bank_mask:0xf
	v_max_f32_dpp v12, v12, v12 quad_perm:[2,3,0,1] row_mask:0xf bank_mask:0xf
	v_max_f32_dpp v13, v13, v13 quad_perm:[2,3,0,1] row_mask:0xf bank_mask:0xf
	v_max_f32_dpp v8, v8, v8 row_half_mirror row_mask:0xf bank_mask:0xf
	v_max_f32_dpp v11, v11, v11 row_half_mirror row_mask:0xf bank_mask:0xf
	v_max_f32_dpp v12, v12, v12 row_half_mirror row_mask:0xf bank_mask:0xf
	v_max_f32_dpp v13, v13, v13 row_half_mirror row_mask:0xf bank_mask:0xf
	v_max_f32_dpp v8, v8, v8 row_mirror row_mask:0xf bank_mask:0xf
	v_max_f32_dpp v11, v11, v11 row_mirror row_mask:0xf bank_mask:0xf
	v_max_f32_dpp v12, v12, v12 row_mirror row_mask:0xf bank_mask:0xf
	v_max_f32_dpp v13, v13, v13 row_mirror row_mask:0xf bank_mask:0xf
	s_nop 0
	ds_swizzle_b32 v232, v8 offset:swizzle(SWAP,16)
	ds_swizzle_b32 v233, v11 offset:swizzle(SWAP,16)
	ds_swizzle_b32 v234, v12 offset:swizzle(SWAP,16)
	ds_swizzle_b32 v235, v13 offset:swizzle(SWAP,16)
	s_waitcnt lgkmcnt(0)
	v_max_f32_e32 v10, v8, v232
	v_rcp_f32_e32 v8, v10
	v_cmp_lt_f32_e32 vcc, 0, v10
	s_waitcnt lgkmcnt(0)
	v_max_f32_e32 v11, v11, v233
	s_waitcnt lgkmcnt(0)
	v_max_f32_e32 v12, v12, v234
	v_cndmask_b32_e32 v42, 0, v8, vcc
	v_mul_f32_e32 v3, v42, v3
	v_mul_f32_e32 v6, v42, v6
	v_cvt_pknorm_i16_f32 v6, v3, v6
	v_mul_f32_e32 v3, v42, v7
	v_mul_f32_e32 v7, v42, v9
	v_cvt_pknorm_i16_f32 v7, v3, v7
	v_pk_mul_f32 v[224:225], v[14:15], v[42:43] op_sel_hi:[1,0]
	v_pk_mul_f32 v[226:227], v[16:17], v[42:43] op_sel_hi:[1,0]
	v_cvt_pknorm_i16_f32 v8, v224, v225
	v_cvt_pknorm_i16_f32 v9, v226, v227
	v_rcp_f32_e32 v3, v11
	v_cmp_lt_f32_e32 vcc, 0, v11
	v_lshl_add_u64 v[14:15], v[4:5], 0, s[6:7]
	global_store_dwordx4 v[14:15], v[6:9], off sc0 sc1
	s_mov_b64 s[6:7], 0x7200
	v_cndmask_b32_e32 v3, 0, v3, vcc
	v_pk_mul_f32 v[228:229], v[18:19], v[2:3] op_sel:[0,1] op_sel_hi:[1,1]
	v_pk_mul_f32 v[230:231], v[20:21], v[2:3] op_sel:[0,1] op_sel_hi:[1,1]
	v_cvt_pknorm_i16_f32 v6, v228, v229
	v_cvt_pknorm_i16_f32 v7, v230, v231
	v_pk_mul_f32 v[224:225], v[22:23], v[2:3] op_sel:[0,1] op_sel_hi:[1,1]
	v_pk_mul_f32 v[226:227], v[24:25], v[2:3] op_sel:[0,1] op_sel_hi:[1,1]
	v_cvt_pknorm_i16_f32 v8, v224, v225
	v_cvt_pknorm_i16_f32 v9, v226, v227
	v_rcp_f32_e32 v3, v12
	v_cmp_lt_f32_e32 vcc, 0, v12
	v_lshl_add_u64 v[14:15], v[4:5], 0, s[6:7]
	global_store_dwordx4 v[14:15], v[6:9], off sc0 sc1
	s_nop 1
	v_pk_mul_f32 v[6:7], v[10:11], s[4:5] op_sel_hi:[1,0]
	v_cndmask_b32_e32 v3, 0, v3, vcc
	global_store_dwordx2 v0, v[6:7], s[2:3] offset:224
	v_pk_mul_f32 v[228:229], v[26:27], v[2:3] op_sel:[0,1] op_sel_hi:[1,1]
	v_pk_mul_f32 v[230:231], v[28:29], v[2:3] op_sel:[0,1] op_sel_hi:[1,1]
	v_cvt_pknorm_i16_f32 v6, v228, v229
	v_cvt_pknorm_i16_f32 v7, v230, v231
	v_pk_mul_f32 v[224:225], v[30:31], v[2:3] op_sel:[0,1] op_sel_hi:[1,1]
	v_pk_mul_f32 v[226:227], v[32:33], v[2:3] op_sel:[0,1] op_sel_hi:[1,1]
	v_cvt_pknorm_i16_f32 v8, v224, v225
	s_waitcnt lgkmcnt(0)
	v_max_f32_e32 v13, v13, v235
	v_cvt_pknorm_i16_f32 v9, v226, v227
	v_rcp_f32_e32 v3, v13
	v_cmp_lt_f32_e32 vcc, 0, v13
	s_mov_b64 s[6:7], 0x7400
	v_lshl_add_u64 v[10:11], v[4:5], 0, s[6:7]
	v_cndmask_b32_e32 v3, 0, v3, vcc
	global_store_dwordx4 v[10:11], v[6:9], off sc0 sc1
	v_pk_mul_f32 v[228:229], v[34:35], v[2:3] op_sel:[0,1] op_sel_hi:[1,1]
	v_pk_mul_f32 v[230:231], v[36:37], v[2:3] op_sel:[0,1] op_sel_hi:[1,1]
	v_cvt_pknorm_i16_f32 v6, v228, v229
	v_cvt_pknorm_i16_f32 v7, v230, v231
	v_pk_mul_f32 v[224:225], v[38:39], v[2:3] op_sel:[0,1] op_sel_hi:[1,1]
	v_pk_mul_f32 v[226:227], v[40:41], v[2:3] op_sel:[0,1] op_sel_hi:[1,1]
	v_cvt_pknorm_i16_f32 v8, v224, v225
	s_mov_b64 s[6:7], 0x7600
	v_cvt_pknorm_i16_f32 v9, v226, v227
	v_lshl_add_u64 v[4:5], v[4:5], 0, s[6:7]
	global_store_dwordx4 v[4:5], v[6:9], off sc0 sc1
	v_pk_mul_f32 v[4:5], v[12:13], s[4:5] op_sel_hi:[1,0]
	global_store_dwordx2 v0, v[4:5], s[2:3] offset:232
	ds_bpermute_b32 v4, v133, v134
	ds_bpermute_b32 v224, v133, v135
	s_lshl_b64 s[0:1], s[0:1], 2
	s_add_u32 s0, s26, s0
	s_addc_u32 s1, s27, s1
	v_mov_b32_e32 v3, v1
	v_cmp_gt_i32_e32 vcc, 32, v132
	v_lshl_add_u64 v[0:1], s[0:1], 0, v[2:3]
	s_and_saveexec_b64 s[0:1], vcc
	s_cbranch_execz .LBB1_8
	s_waitcnt lgkmcnt(0)
	v_add_f32_e32 v2, v134, v4
	v_add_f32_e32 v3, v135, v224
	global_store_dword v[0:1], v2, off
	global_store_dword v[0:1], v3, off offset:128
